# speedup vs baseline: 1.0407x; 1.0163x over previous
_Z16closed_form_mainPKfS0_PKiPf:
	s_load_dwordx8 s[16:23], s[0:1], 0x0
	s_lshr_b32 s6, s2, 3
	v_readfirstlane_b32 s0, v0
	s_mul_hi_u32 s7, s6, 0x24924925
	s_lshr_b32 s4, s0, 6
	s_and_b32 s0, s2, 7
	s_mul_i32 s1, s7, 7
	s_bfe_u32 s5, s2, 0x10003
	s_sub_i32 s1, s6, s1
	s_mul_i32 s36, s0, 7
	s_xor_b32 s3, s4, s5
	s_add_i32 s36, s36, s1
	s_waitcnt lgkmcnt(0)
	s_mov_b64 s[28:29], s[22:23]
	v_and_b32_e32 v19, 63, v0
	s_cmp_lt_u32 s36, 52
	s_mov_b64 s[0:1], -1
	s_cbranch_scc0 .LBB0_32
	s_mul_hi_u32 s0, s6, 0x20820821
	s_lshr_b32 s38, s0, 3
	s_mul_hi_u32 s0, s7, 0x1c71c71d
	s_mul_i32 s0, s0, 9
	s_sub_i32 s0, s7, s0
	v_add_u32_e32 v2, -3, v19
	v_mad_u64_u32 v[0:1], s[0:1], s0, 57, v[2:3]
	s_mov_b64 s[24:25], s[18:19]
	v_mov_b32_e32 v1, 0x200
	v_med3_i32 v1, v0, 0, v1
	s_mul_i32 s34, s36, 10
	s_and_b32 s17, s17, 0xffff
	s_and_b32 s25, s25, 0xffff
	v_cmp_gt_u32_e64 s[0:1], 57, v2
	s_mov_b32 s19, 0x20000
	s_mov_b32 s18, 0xe0e038
	s_mov_b32 s26, 0x606018
	s_mul_i32 s35, s38, 0x70701c
	s_mul_i32 s33, s38, 0x30300c
	v_lshlrev_b32_e32 v28, 2, v1
	v_mul_u32_u24_e32 v27, 12, v1
	v_lshlrev_b32_e32 v23, 4, v19
	s_cmp_lg_u32 s4, s5
	v_sub_u32_e64 v29, s34, 2 clamp
	s_cbranch_scc0 .LBB0_15
	s_setprio 2
	s_mov_b32 s27, s19
	s_and_b32 s21, s21, 0xffff
	s_mov_b32 s22, 0x202008
	s_mov_b32 s23, s19
	s_mul_i32 s38, s38, 0x101004
	s_movk_i32 s37, 0x80
	v_add_u32_e32 v18, -1, v0
	s_movk_i32 s4, 0x201
	s_movk_i32 s5, 0x1ff
	v_cmp_gt_u32_e64 s[40:41], s4, v0
	v_cmp_gt_u32_e64 s[42:43], s5, v18
	v_mov_b32_e32 v18, 0x42c80000
	v_mov_b32_e32 v22, 0x3de38e39
	v_mov_b32_e32 v26, 0x3a3d6628
	v_mov_b32_e32 v1, 0
	s_add_i32 s4, s34, -3
	s_max_i32 s4, s4, 0
	s_mul_i32 s4, s4, 0x804
	s_add_i32 s4, s4, s38
	buffer_load_dword v29, v28, s[20:23], s4 offen nt
	s_add_i32 s4, s34, -2
	s_max_i32 s4, s4, 0
	s_mul_i32 s4, s4, 0x804
	s_add_i32 s4, s4, s38
	buffer_load_dword v2, v28, s[20:23], s4 offen nt
	s_add_i32 s5, s34, -2
	s_max_i32 s5, s5, 0
	s_mul_i32 s6, s5, 0x804
	s_add_i32 s6, s6, s35
	s_add_i32 s7, s6, 0x505014
	s_add_i32 s8, s6, 0x606018
	s_mul_i32 s9, s5, 0x180c
	s_add_i32 s9, s9, s33
	s_add_i32 s4, s34, -1
	s_max_i32 s4, s4, 0
	s_mul_i32 s4, s4, 0x804
	s_add_i32 s4, s4, s38
	buffer_load_dword v3, v28, s[20:23], s4 offen nt
	buffer_load_dwordx3 v[8:10], v27, s[24:27], s9 offen nt
	buffer_load_dword v4, v28, s[16:19], s7 offen nt
	buffer_load_dword v5, v28, s[16:19], s8 offen nt
	s_add_i32 s5, s34, -1
	s_max_i32 s5, s5, 0
	s_mul_i32 s6, s5, 0x804
	s_add_i32 s6, s6, s35
	s_add_i32 s7, s6, 0x505014
	s_add_i32 s8, s6, 0x606018
	s_mul_i32 s9, s5, 0x180c
	s_add_i32 s9, s9, s33
	s_add_i32 s4, s34, 0
	s_min_i32 s4, s4, 0x200
	s_mul_i32 s4, s4, 0x804
	s_add_i32 s4, s4, s38
	buffer_load_dword v16, v28, s[20:23], s4 offen nt
	buffer_load_dwordx3 v[12:14], v27, s[24:27], s9 offen nt
	buffer_load_dword v6, v28, s[16:19], s7 offen nt
	buffer_load_dword v7, v28, s[16:19], s8 offen nt
	s_waitcnt vmcnt(8)
	s_add_i32 s4, s34, -3
	s_cmpk_lt_u32 s4, 0x201
	s_cselect_b64 s[12:13], s[40:41], 0
	v_cmp_eq_u32_e64 s[14:15], s37, v29
	s_and_b64 s[14:15], s[14:15], s[12:13]
	v_cndmask_b32_e64 v17, 0, 1, s[14:15]
	s_add_i32 s4, s34, -2
	s_cmpk_lt_u32 s4, 0x201
	s_cselect_b64 s[12:13], s[40:41], 0
	v_cmp_eq_u32_e64 s[14:15], s37, v2
	s_and_b64 s[14:15], s[14:15], s[12:13]
	v_cndmask_b32_e64 v20, 0, 1, s[14:15]
	s_nop 0
	v_or_b32_dpp v21, v17, v17 wave_shr:1 row_mask:0xf bank_mask:0xf bound_ctrl:1
	v_or_b32_dpp v24, v20, v20 wave_shr:1 row_mask:0xf bank_mask:0xf bound_ctrl:1
	s_nop 1
	v_or_b32_dpp v21, v17, v21 wave_shl:1 row_mask:0xf bank_mask:0xf bound_ctrl:1
	v_or_b32_dpp v24, v20, v24 wave_shl:1 row_mask:0xf bank_mask:0xf bound_ctrl:1
	s_nop 1
	v_or_b32_dpp v25, v21, v21 wave_shr:1 row_mask:0xf bank_mask:0xf bound_ctrl:1
	v_or_b32_dpp v30, v24, v24 wave_shr:1 row_mask:0xf bank_mask:0xf bound_ctrl:1
	s_nop 1
	v_or_b32_dpp v25, v21, v25 wave_shl:1 row_mask:0xf bank_mask:0xf bound_ctrl:1
	v_or_b32_dpp v30, v24, v30 wave_shl:1 row_mask:0xf bank_mask:0xf bound_ctrl:1
	v_mov_b32_e32 v17, 0
	v_mov_b32_e32 v24, 0
	s_add_i32 s5, s34, 0
	s_min_i32 s5, s5, 0x200
	s_mul_i32 s6, s5, 0x804
	s_add_i32 s6, s6, s35
	s_add_i32 s7, s6, 0x505014
	s_add_i32 s8, s6, 0x606018
	s_mul_i32 s9, s5, 0x180c
	s_add_i32 s9, s9, s33
	s_add_i32 s4, s34, 1
	s_min_i32 s4, s4, 0x200
	s_mul_i32 s4, s4, 0x804
	s_add_i32 s4, s4, s38
	buffer_load_dword v31, v28, s[20:23], s4 offen nt
	buffer_load_dwordx3 v[32:34], v27, s[24:27], s9 offen nt
	buffer_load_dword v20, v28, s[16:19], s7 offen nt
	buffer_load_dword v21, v28, s[16:19], s8 offen nt
	s_waitcnt vmcnt(8)
	v_mov_b32_dpp v36, v8 wave_shr:1 row_mask:0xf bank_mask:0xf bound_ctrl:1
	v_mov_b32_dpp v37, v9 wave_shr:1 row_mask:0xf bank_mask:0xf bound_ctrl:1
	v_mov_b32_dpp v38, v10 wave_shr:1 row_mask:0xf bank_mask:0xf bound_ctrl:1
	v_mov_b32_dpp v40, v8 wave_shl:1 row_mask:0xf bank_mask:0xf bound_ctrl:1
	v_mov_b32_dpp v41, v9 wave_shl:1 row_mask:0xf bank_mask:0xf bound_ctrl:1
	v_mov_b32_dpp v42, v10 wave_shl:1 row_mask:0xf bank_mask:0xf bound_ctrl:1
	s_add_i32 s4, s34, -1
	s_cmpk_lt_u32 s4, 0x201
	s_cselect_b64 s[12:13], s[40:41], 0
	v_cmp_eq_u32_e64 s[14:15], s37, v3
	s_and_b64 s[14:15], s[14:15], s[12:13]
	v_cndmask_b32_e64 v44, 0, 1, s[14:15]
	v_mul_f32_e64 v46, v8, v8
	v_mul_f32_e64 v47, v8, v9
	v_mul_f32_e64 v48, v8, v10
	v_mul_f32_e64 v49, v9, v9
	v_mul_f32_e64 v50, v9, v10
	v_mul_f32_e64 v51, v10, v10
	v_or_b32_dpp v45, v44, v44 wave_shr:1 row_mask:0xf bank_mask:0xf bound_ctrl:1
	s_nop 1
	v_or_b32_dpp v45, v44, v45 wave_shl:1 row_mask:0xf bank_mask:0xf bound_ctrl:1
	s_nop 1
	v_or_b32_dpp v52, v45, v45 wave_shr:1 row_mask:0xf bank_mask:0xf bound_ctrl:1
	s_nop 1
	v_or_b32_dpp v52, v45, v52 wave_shl:1 row_mask:0xf bank_mask:0xf bound_ctrl:1
	v_or3_b32 v53, v52, v30, v25
	v_or3_b32 v53, v53, v17, v24
	s_add_i32 s4, s34, -4
	s_cmpk_lt_u32 s4, 0x1ff
	s_cselect_b64 s[12:13], s[42:43], 0
	v_cmp_ne_u32_e64 s[30:31], 0, v53
	s_and_b64 s[30:31], s[30:31], s[12:13]
	v_cndmask_b32_e64 v53, 0, 1.0, s[30:31]
	v_add_f32_e64 v44, v8, v36
	v_add_f32_e64 v45, v9, v37
	v_add_f32_e64 v54, v10, v38
	v_fma_f32 v46, v36, v36, v46
	v_fma_f32 v47, v36, v37, v47
	v_fma_f32 v48, v36, v38, v48
	v_fma_f32 v49, v37, v37, v49
	v_fma_f32 v50, v37, v38, v50
	v_fma_f32 v51, v38, v38, v51
	v_add_f32_dpp v61, v53, v53 wave_shr:1 row_mask:0xf bank_mask:0xf bound_ctrl:1
	v_add_f32_e64 v44, v44, v40
	v_add_f32_e64 v45, v45, v41
	v_add_f32_e64 v54, v54, v42
	v_fma_f32 v55, v40, v40, v46
	v_fma_f32 v56, v40, v41, v47
	v_fma_f32 v57, v40, v42, v48
	v_fma_f32 v58, v41, v41, v49
	v_fma_f32 v59, v41, v42, v50
	v_fma_f32 v60, v42, v42, v51
	v_add_f32_dpp v61, v53, v61 wave_shl:1 row_mask:0xf bank_mask:0xf bound_ctrl:1
	v_mov_b32_dpp v46, v4 wave_shr:1 row_mask:0xf bank_mask:0xf bound_ctrl:1
	v_mov_b32_dpp v47, v5 wave_shr:1 row_mask:0xf bank_mask:0xf bound_ctrl:1
	v_mov_b32_dpp v48, v4 wave_shl:1 row_mask:0xf bank_mask:0xf bound_ctrl:1
	v_mov_b32_dpp v49, v5 wave_shl:1 row_mask:0xf bank_mask:0xf bound_ctrl:1
	v_pk_mul_f32 v[50:51], v[4:5], v[8:9] op_sel_hi:[1,0]
	v_pk_mul_f32 v[62:63], v[4:5], v[8:9] op_sel:[0,1]
	v_pk_mul_f32 v[64:65], v[4:5], v[10:11] op_sel_hi:[1,0]
	v_pk_add_f32 v[66:67], v[4:5], v[46:47]
	v_pk_fma_f32 v[50:51], v[46:47], v[36:37], v[50:51] op_sel_hi:[1,0,1]
	v_pk_fma_f32 v[62:63], v[46:47], v[36:37], v[62:63] op_sel:[0,1,0]
	v_pk_fma_f32 v[64:65], v[46:47], v[38:39], v[64:65] op_sel_hi:[1,0,1]
	v_pk_add_f32 v[66:67], v[66:67], v[48:49]
	v_pk_fma_f32 v[50:51], v[48:49], v[40:41], v[50:51] op_sel_hi:[1,0,1]
	v_pk_fma_f32 v[62:63], v[48:49], v[40:41], v[62:63] op_sel:[0,1,0]
	v_pk_fma_f32 v[64:65], v[48:49], v[42:43], v[64:65] op_sel_hi:[1,0,1]
	s_barrier
	s_add_i32 s5, s34, 1
	s_min_i32 s5, s5, 0x200
	s_mul_i32 s6, s5, 0x804
	s_add_i32 s6, s6, s35
	s_add_i32 s7, s6, 0x505014
	s_add_i32 s8, s6, 0x606018
	s_mul_i32 s9, s5, 0x180c
	s_add_i32 s9, s9, s33
	s_add_i32 s4, s34, 2
	s_min_i32 s4, s4, 0x200
	s_mul_i32 s4, s4, 0x804
	s_add_i32 s4, s4, s38
	buffer_load_dword v24, v28, s[20:23], s4 offen nt
	buffer_load_dwordx3 v[68:70], v27, s[24:27], s9 offen nt
	buffer_load_dword v46, v28, s[16:19], s7 offen nt
	buffer_load_dword v47, v28, s[16:19], s8 offen nt
	s_waitcnt vmcnt(8)
	v_mov_b32_dpp v72, v12 wave_shr:1 row_mask:0xf bank_mask:0xf bound_ctrl:1
	v_mov_b32_dpp v73, v13 wave_shr:1 row_mask:0xf bank_mask:0xf bound_ctrl:1
	v_mov_b32_dpp v74, v14 wave_shr:1 row_mask:0xf bank_mask:0xf bound_ctrl:1
	v_mov_b32_dpp v76, v12 wave_shl:1 row_mask:0xf bank_mask:0xf bound_ctrl:1
	v_mov_b32_dpp v77, v13 wave_shl:1 row_mask:0xf bank_mask:0xf bound_ctrl:1
	v_mov_b32_dpp v78, v14 wave_shl:1 row_mask:0xf bank_mask:0xf bound_ctrl:1
	s_add_i32 s4, s34, 0
	s_cmpk_lt_u32 s4, 0x201
	s_cselect_b64 s[12:13], s[40:41], 0
	v_cmp_eq_u32_e64 s[14:15], s37, v16
	s_and_b64 s[14:15], s[14:15], s[12:13]
	v_cndmask_b32_e64 v53, 0, 1, s[14:15]
	v_mul_f32_e64 v48, v12, v12
	v_mul_f32_e64 v49, v12, v13
	v_mul_f32_e64 v80, v12, v14
	v_mul_f32_e64 v81, v13, v13
	v_mul_f32_e64 v82, v13, v14
	v_mul_f32_e64 v83, v14, v14
	v_or_b32_dpp v84, v53, v53 wave_shr:1 row_mask:0xf bank_mask:0xf bound_ctrl:1
	s_nop 1
	v_or_b32_dpp v84, v53, v84 wave_shl:1 row_mask:0xf bank_mask:0xf bound_ctrl:1
	s_nop 1
	v_or_b32_dpp v85, v84, v84 wave_shr:1 row_mask:0xf bank_mask:0xf bound_ctrl:1
	s_nop 1
	v_or_b32_dpp v85, v84, v85 wave_shl:1 row_mask:0xf bank_mask:0xf bound_ctrl:1
	v_or3_b32 v53, v85, v52, v30
	v_or3_b32 v53, v53, v25, v17
	s_add_i32 s4, s34, -3
	s_cmpk_lt_u32 s4, 0x1ff
	s_cselect_b64 s[12:13], s[42:43], 0
	v_cmp_ne_u32_e64 s[30:31], 0, v53
	s_and_b64 s[30:31], s[30:31], s[12:13]
	v_cndmask_b32_e64 v53, 0, 1.0, s[30:31]
	v_add_f32_e64 v86, v12, v72
	v_add_f32_e64 v87, v13, v73
	v_add_f32_e64 v88, v14, v74
	v_fma_f32 v48, v72, v72, v48
	v_fma_f32 v49, v72, v73, v49
	v_fma_f32 v80, v72, v74, v80
	v_fma_f32 v81, v73, v73, v81
	v_fma_f32 v82, v73, v74, v82
	v_fma_f32 v83, v74, v74, v83
	v_add_f32_dpp v95, v53, v53 wave_shr:1 row_mask:0xf bank_mask:0xf bound_ctrl:1
	v_add_f32_e64 v86, v86, v76
	v_add_f32_e64 v87, v87, v77
	v_add_f32_e64 v88, v88, v78
	v_fma_f32 v89, v76, v76, v48
	v_fma_f32 v90, v76, v77, v49
	v_fma_f32 v91, v76, v78, v80
	v_fma_f32 v92, v77, v77, v81
	v_fma_f32 v93, v77, v78, v82
	v_fma_f32 v94, v78, v78, v83
	v_add_f32_dpp v95, v53, v95 wave_shl:1 row_mask:0xf bank_mask:0xf bound_ctrl:1
	v_mov_b32_dpp v48, v6 wave_shr:1 row_mask:0xf bank_mask:0xf bound_ctrl:1
	v_mov_b32_dpp v49, v7 wave_shr:1 row_mask:0xf bank_mask:0xf bound_ctrl:1
	v_mov_b32_dpp v80, v6 wave_shl:1 row_mask:0xf bank_mask:0xf bound_ctrl:1
	v_mov_b32_dpp v81, v7 wave_shl:1 row_mask:0xf bank_mask:0xf bound_ctrl:1
	v_pk_mul_f32 v[82:83], v[6:7], v[12:13] op_sel_hi:[1,0]
	v_pk_mul_f32 v[96:97], v[6:7], v[12:13] op_sel:[0,1]
	v_pk_mul_f32 v[98:99], v[6:7], v[14:15] op_sel_hi:[1,0]
	v_pk_add_f32 v[100:101], v[6:7], v[48:49]
	v_pk_fma_f32 v[82:83], v[48:49], v[72:73], v[82:83] op_sel_hi:[1,0,1]
	v_pk_fma_f32 v[96:97], v[48:49], v[72:73], v[96:97] op_sel:[0,1,0]
	v_pk_fma_f32 v[98:99], v[48:49], v[74:75], v[98:99] op_sel_hi:[1,0,1]
	v_pk_add_f32 v[100:101], v[100:101], v[80:81]
	v_pk_fma_f32 v[82:83], v[80:81], v[76:77], v[82:83] op_sel_hi:[1,0,1]
	v_pk_fma_f32 v[96:97], v[80:81], v[76:77], v[96:97] op_sel:[0,1,0]
	v_pk_fma_f32 v[98:99], v[80:81], v[78:79], v[98:99] op_sel_hi:[1,0,1]
	s_barrier
	s_add_i32 s5, s34, 2
	s_min_i32 s5, s5, 0x200
	s_mul_i32 s6, s5, 0x804
	s_add_i32 s6, s6, s35
	s_add_i32 s7, s6, 0x505014
	s_add_i32 s8, s6, 0x606018
	s_mul_i32 s9, s5, 0x180c
	s_add_i32 s9, s9, s33
	s_add_i32 s4, s34, 3
	s_min_i32 s4, s4, 0x200
	s_mul_i32 s4, s4, 0x804
	s_add_i32 s4, s4, s38
	buffer_load_dword v17, v28, s[20:23], s4 offen nt
	buffer_load_dwordx3 v[104:106], v27, s[24:27], s9 offen nt
	buffer_load_dword v48, v28, s[16:19], s7 offen nt
	buffer_load_dword v49, v28, s[16:19], s8 offen nt
	s_waitcnt vmcnt(8)
	v_mov_b32_dpp v108, v32 wave_shr:1 row_mask:0xf bank_mask:0xf bound_ctrl:1
	v_mov_b32_dpp v109, v33 wave_shr:1 row_mask:0xf bank_mask:0xf bound_ctrl:1
	v_mov_b32_dpp v110, v34 wave_shr:1 row_mask:0xf bank_mask:0xf bound_ctrl:1
	v_mov_b32_dpp v112, v32 wave_shl:1 row_mask:0xf bank_mask:0xf bound_ctrl:1
	v_mov_b32_dpp v113, v33 wave_shl:1 row_mask:0xf bank_mask:0xf bound_ctrl:1
	v_mov_b32_dpp v114, v34 wave_shl:1 row_mask:0xf bank_mask:0xf bound_ctrl:1
	s_add_i32 s4, s34, 1
	s_cmpk_lt_u32 s4, 0x201
	s_cselect_b64 s[12:13], s[40:41], 0
	v_cmp_eq_u32_e64 s[14:15], s37, v31
	s_and_b64 s[14:15], s[14:15], s[12:13]
	v_cndmask_b32_e64 v29, 0, 1, s[14:15]
	v_mul_f32_e64 v80, v32, v32
	v_mul_f32_e64 v81, v32, v33
	v_mul_f32_e64 v102, v32, v34
	v_mul_f32_e64 v103, v33, v33
	v_mul_f32_e64 v116, v33, v34
	v_mul_f32_e64 v117, v34, v34
	v_or_b32_dpp v53, v29, v29 wave_shr:1 row_mask:0xf bank_mask:0xf bound_ctrl:1
	s_nop 1
	v_or_b32_dpp v53, v29, v53 wave_shl:1 row_mask:0xf bank_mask:0xf bound_ctrl:1
	s_nop 1
	v_or_b32_dpp v84, v53, v53 wave_shr:1 row_mask:0xf bank_mask:0xf bound_ctrl:1
	s_nop 1
	v_or_b32_dpp v84, v53, v84 wave_shl:1 row_mask:0xf bank_mask:0xf bound_ctrl:1
	v_or3_b32 v29, v84, v85, v52
	v_or3_b32 v29, v29, v30, v25
	s_add_i32 s4, s34, -2
	s_cmpk_lt_u32 s4, 0x1ff
	s_cselect_b64 s[12:13], s[42:43], 0
	v_cmp_ne_u32_e64 s[30:31], 0, v29
	s_and_b64 s[30:31], s[30:31], s[12:13]
	v_cndmask_b32_e64 v29, 0, 1.0, s[30:31]
	v_add_f32_e64 v118, v32, v108
	v_add_f32_e64 v119, v33, v109
	v_add_f32_e64 v120, v34, v110
	v_fma_f32 v80, v108, v108, v80
	v_fma_f32 v81, v108, v109, v81
	v_fma_f32 v102, v108, v110, v102
	v_fma_f32 v103, v109, v109, v103
	v_fma_f32 v116, v109, v110, v116
	v_fma_f32 v117, v110, v110, v117
	v_add_f32_dpp v127, v29, v29 wave_shr:1 row_mask:0xf bank_mask:0xf bound_ctrl:1
	v_add_f32_e64 v118, v118, v112
	v_add_f32_e64 v119, v119, v113
	v_add_f32_e64 v120, v120, v114
	v_fma_f32 v121, v112, v112, v80
	v_fma_f32 v122, v112, v113, v81
	v_fma_f32 v123, v112, v114, v102
	v_fma_f32 v124, v113, v113, v103
	v_fma_f32 v125, v113, v114, v116
	v_fma_f32 v126, v114, v114, v117
	v_add_f32_dpp v127, v29, v127 wave_shl:1 row_mask:0xf bank_mask:0xf bound_ctrl:1
	v_pk_add_f32 v[80:81], v[86:87], v[118:119]
	v_pk_add_f32 v[102:103], v[44:45], v[80:81]
	v_pk_add_f32 v[44:45], v[88:89], v[120:121]
	v_pk_add_f32 v[86:87], v[54:55], v[44:45]
	v_pk_add_f32 v[54:55], v[90:91], v[122:123]
	v_pk_add_f32 v[88:89], v[56:57], v[54:55]
	v_pk_add_f32 v[56:57], v[92:93], v[124:125]
	v_pk_add_f32 v[90:91], v[58:59], v[56:57]
	v_pk_add_f32 v[58:59], v[94:95], v[126:127]
	v_pk_add_f32 v[92:93], v[60:61], v[58:59]
	v_mul_f32_e64 v128, v102, v22
	v_mul_f32_e64 v129, v103, v22
	v_mul_f32_e64 v130, v86, v22
	v_fma_f32 v29, v87, v22, v26
	v_mul_f32_e64 v53, v88, v22
	v_mul_f32_e64 v60, v89, v22
	v_fma_f32 v61, v90, v22, v26
	v_mul_f32_e64 v94, v91, v22
	v_fma_f32 v95, v92, v22, v26
	v_fma_f32 v29, -v128, v128, v29
	v_fma_f32 v53, -v128, v129, v53
	v_fma_f32 v60, -v128, v130, v60
	v_fma_f32 v61, -v129, v129, v61
	v_fma_f32 v94, -v129, v130, v94
	v_fma_f32 v95, -v130, v130, v95
	v_mul_f32_e64 v116, v94, v94
	v_mul_f32_e64 v117, v53, v95
	v_mul_f32_e64 v140, v60, v61
	v_mul_f32_e64 v141, v60, v60
	v_mul_f32_e64 v142, v29, v94
	v_mul_f32_e64 v143, v53, v53
	v_fma_f32 v116, v61, v95, -v116
	v_fma_f32 v117, v60, v94, -v117
	v_fma_f32 v140, v53, v94, -v140
	v_fma_f32 v141, v29, v95, -v141
	v_fma_f32 v142, v53, v60, -v142
	v_fma_f32 v143, v29, v61, -v143
	v_mul_f32_e64 v144, v29, v116
	v_fma_f32 v144, v53, v117, v144
	v_fma_f32 v144, v60, v140, v144
	v_rcp_f32_e32 v144, v144
	v_cmp_ne_u32_e64 vcc, s37, v2
	v_mul_f32_e64 v144, v144, v22
	v_cndmask_b32_e64 v144, 0, v144, s[30:31]
	v_cndmask_b32_e64 v29, 0, v18, vcc
	v_cndmask_b32_e64 v137, 0, v22, s[30:31]
	v_mul_f32_e64 v131, v116, v144
	v_mul_f32_e64 v132, v117, v144
	v_mul_f32_e64 v133, v140, v144
	v_mul_f32_e64 v134, v141, v144
	v_mul_f32_e64 v135, v142, v144
	v_mul_f32_e64 v136, v143, v144
	v_add_f32_e64 v138, v93, v29
	v_mov_b32_e32 v139, v2
	ds_write_b128 v23, v[128:131]
	ds_write_b128 v23, v[132:135] offset:1024
	ds_write_b128 v23, v[136:139] offset:2048
	v_mov_b32_dpp v60, v20 wave_shr:1 row_mask:0xf bank_mask:0xf bound_ctrl:1
	v_mov_b32_dpp v61, v21 wave_shr:1 row_mask:0xf bank_mask:0xf bound_ctrl:1
	v_mov_b32_dpp v86, v20 wave_shl:1 row_mask:0xf bank_mask:0xf bound_ctrl:1
	v_mov_b32_dpp v87, v21 wave_shl:1 row_mask:0xf bank_mask:0xf bound_ctrl:1
	v_pk_mul_f32 v[88:89], v[20:21], v[32:33] op_sel_hi:[1,0]
	v_pk_mul_f32 v[90:91], v[20:21], v[32:33] op_sel:[0,1]
	v_pk_mul_f32 v[92:93], v[20:21], v[34:35] op_sel_hi:[1,0]
	v_pk_add_f32 v[94:95], v[20:21], v[60:61]
	v_pk_fma_f32 v[88:89], v[60:61], v[108:109], v[88:89] op_sel_hi:[1,0,1]
	v_pk_fma_f32 v[90:91], v[60:61], v[108:109], v[90:91] op_sel:[0,1,0]
	v_pk_fma_f32 v[92:93], v[60:61], v[110:111], v[92:93] op_sel_hi:[1,0,1]
	v_pk_add_f32 v[94:95], v[94:95], v[86:87]
	v_pk_fma_f32 v[88:89], v[86:87], v[112:113], v[88:89] op_sel_hi:[1,0,1]
	v_pk_fma_f32 v[90:91], v[86:87], v[112:113], v[90:91] op_sel:[0,1,0]
	v_pk_fma_f32 v[92:93], v[86:87], v[114:115], v[92:93] op_sel_hi:[1,0,1]
	s_waitcnt lgkmcnt(0)
	s_barrier
	v_pk_add_f32 v[60:61], v[100:101], v[94:95]
	v_pk_add_f32 v[86:87], v[66:67], v[60:61]
	v_pk_add_f32 v[66:67], v[82:83], v[88:89]
	v_pk_add_f32 v[100:101], v[50:51], v[66:67]
	v_pk_add_f32 v[50:51], v[96:97], v[90:91]
	v_pk_add_f32 v[82:83], v[62:63], v[50:51]
	v_pk_add_f32 v[62:63], v[98:99], v[92:93]
	v_pk_add_f32 v[96:97], v[64:65], v[62:63]
	v_pk_fma_f32 v[100:101], v[128:129], v[86:87], v[100:101] op_sel_hi:[0,1,1] neg_lo:[1,0,0] neg_hi:[1,0,0]
	v_pk_fma_f32 v[82:83], v[128:129], v[86:87], v[82:83] op_sel:[1,0,0] neg_lo:[1,0,0] neg_hi:[1,0,0]
	v_pk_fma_f32 v[96:97], v[130:131], v[86:87], v[96:97] op_sel_hi:[0,1,1] neg_lo:[1,0,0] neg_hi:[1,0,0]
	v_pk_mul_f32 v[64:65], v[130:131], v[100:101] op_sel:[1,0]
	v_pk_mul_f32 v[98:99], v[132:133], v[100:101] op_sel_hi:[0,1]
	v_pk_mul_f32 v[102:103], v[132:133], v[100:101] op_sel:[1,0]
	v_pk_fma_f32 v[64:65], v[132:133], v[82:83], v[64:65] op_sel_hi:[0,1,1]
	v_pk_fma_f32 v[98:99], v[134:135], v[82:83], v[98:99] op_sel_hi:[0,1,1]
	v_pk_fma_f32 v[102:103], v[134:135], v[82:83], v[102:103] op_sel:[1,0,0]
	v_pk_fma_f32 v[64:65], v[132:133], v[96:97], v[64:65] op_sel:[1,0,0]
	v_pk_fma_f32 v[98:99], v[134:135], v[96:97], v[98:99] op_sel:[1,0,0]
	v_pk_fma_f32 v[102:103], v[136:137], v[96:97], v[102:103] op_sel_hi:[0,1,1]
	v_pk_mul_f32 v[116:117], v[128:129], v[64:65] op_sel_hi:[0,1]
	v_pk_fma_f32 v[116:117], v[128:129], v[98:99], v[116:117] op_sel:[1,0,0]
	v_pk_fma_f32 v[116:117], v[130:131], v[102:103], v[116:117] op_sel_hi:[0,1,1]
	v_pk_fma_f32 v[116:117], v[136:137], v[86:87], v[116:117] op_sel:[1,0,0] neg_lo:[0,0,1] neg_hi:[0,0,1]
	s_add_i32 s5, s34, 3
	s_min_i32 s5, s5, 0x200
	s_mul_i32 s6, s5, 0x804
	s_add_i32 s6, s6, s35
	s_add_i32 s7, s6, 0x505014
	s_add_i32 s8, s6, 0x606018
	s_mul_i32 s9, s5, 0x180c
	s_add_i32 s9, s9, s33
	s_add_i32 s4, s34, 4
	s_min_i32 s4, s4, 0x200
	s_mul_i32 s4, s4, 0x804
	s_add_i32 s4, s4, s38
	buffer_load_dword v2, v28, s[20:23], s4 offen nt
	buffer_load_dwordx3 v[8:10], v27, s[24:27], s9 offen nt
	buffer_load_dword v4, v28, s[16:19], s7 offen nt
	buffer_load_dword v5, v28, s[16:19], s8 offen nt
	s_waitcnt vmcnt(8)
	v_mov_b32_dpp v36, v68 wave_shr:1 row_mask:0xf bank_mask:0xf bound_ctrl:1
	v_mov_b32_dpp v37, v69 wave_shr:1 row_mask:0xf bank_mask:0xf bound_ctrl:1
	v_mov_b32_dpp v38, v70 wave_shr:1 row_mask:0xf bank_mask:0xf bound_ctrl:1
	v_mov_b32_dpp v40, v68 wave_shl:1 row_mask:0xf bank_mask:0xf bound_ctrl:1
	v_mov_b32_dpp v41, v69 wave_shl:1 row_mask:0xf bank_mask:0xf bound_ctrl:1
	v_mov_b32_dpp v42, v70 wave_shl:1 row_mask:0xf bank_mask:0xf bound_ctrl:1
	s_add_i32 s4, s34, 2
	s_cmpk_lt_u32 s4, 0x201
	s_cselect_b64 s[12:13], s[40:41], 0
	v_cmp_eq_u32_e64 s[14:15], s37, v24
	s_and_b64 s[14:15], s[14:15], s[12:13]
	v_cndmask_b32_e64 v25, 0, 1, s[14:15]
	v_mul_f32_e64 v82, v68, v68
	v_mul_f32_e64 v83, v68, v69
	v_mul_f32_e64 v86, v68, v70
	v_mul_f32_e64 v87, v69, v69
	v_mul_f32_e64 v96, v69, v70
	v_mul_f32_e64 v97, v70, v70
	v_or_b32_dpp v29, v25, v25 wave_shr:1 row_mask:0xf bank_mask:0xf bound_ctrl:1
	s_nop 1
	v_or_b32_dpp v29, v25, v29 wave_shl:1 row_mask:0xf bank_mask:0xf bound_ctrl:1
	s_nop 1
	v_or_b32_dpp v53, v29, v29 wave_shr:1 row_mask:0xf bank_mask:0xf bound_ctrl:1
	s_nop 1
	v_or_b32_dpp v53, v29, v53 wave_shl:1 row_mask:0xf bank_mask:0xf bound_ctrl:1
	v_or3_b32 v25, v53, v84, v85
	v_or3_b32 v25, v25, v52, v30
	s_add_i32 s4, s34, -1
	s_cmpk_lt_u32 s4, 0x1ff
	s_cselect_b64 s[12:13], s[42:43], 0
	v_cmp_ne_u32_e64 s[30:31], 0, v25
	s_and_b64 s[30:31], s[30:31], s[12:13]
	v_cndmask_b32_e64 v25, 0, 1.0, s[30:31]
	v_add_f32_e64 v100, v68, v36
	v_add_f32_e64 v101, v69, v37
	v_add_f32_e64 v128, v70, v38
	v_fma_f32 v82, v36, v36, v82
	v_fma_f32 v83, v36, v37, v83
	v_fma_f32 v86, v36, v38, v86
	v_fma_f32 v87, v37, v37, v87
	v_fma_f32 v96, v37, v38, v96
	v_fma_f32 v97, v38, v38, v97
	v_add_f32_dpp v135, v25, v25 wave_shr:1 row_mask:0xf bank_mask:0xf bound_ctrl:1
	v_add_f32_e64 v100, v100, v40
	v_add_f32_e64 v101, v101, v41
	v_add_f32_e64 v128, v128, v42
	v_fma_f32 v129, v40, v40, v82
	v_fma_f32 v130, v40, v41, v83
	v_fma_f32 v131, v40, v42, v86
	v_fma_f32 v132, v41, v41, v87
	v_fma_f32 v133, v41, v42, v96
	v_fma_f32 v134, v42, v42, v97
	v_add_f32_dpp v135, v25, v135 wave_shl:1 row_mask:0xf bank_mask:0xf bound_ctrl:1
	v_pk_add_f32 v[82:83], v[80:81], v[100:101]
	v_pk_add_f32 v[80:81], v[44:45], v[128:129]
	v_pk_add_f32 v[44:45], v[54:55], v[130:131]
	v_pk_add_f32 v[54:55], v[56:57], v[132:133]
	v_pk_add_f32 v[56:57], v[58:59], v[134:135]
	v_mul_f32_e64 v136, v82, v22
	v_mul_f32_e64 v137, v83, v22
	v_mul_f32_e64 v138, v80, v22
	v_fma_f32 v25, v81, v22, v26
	v_mul_f32_e64 v29, v44, v22
	v_mul_f32_e64 v58, v45, v22
	v_fma_f32 v59, v54, v22, v26
	v_mul_f32_e64 v86, v55, v22
	v_fma_f32 v87, v56, v22, v26
	v_fma_f32 v25, -v136, v136, v25
	v_fma_f32 v29, -v136, v137, v29
	v_fma_f32 v58, -v136, v138, v58
	v_fma_f32 v59, -v137, v137, v59
	v_fma_f32 v86, -v137, v138, v86
	v_fma_f32 v87, -v138, v138, v87
	v_mul_f32_e64 v96, v86, v86
	v_mul_f32_e64 v97, v29, v87
	v_mul_f32_e64 v148, v58, v59
	v_mul_f32_e64 v149, v58, v58
	v_mul_f32_e64 v150, v25, v86
	v_mul_f32_e64 v151, v29, v29
	v_fma_f32 v96, v59, v87, -v96
	v_fma_f32 v97, v58, v86, -v97
	v_fma_f32 v148, v29, v86, -v148
	v_fma_f32 v149, v25, v87, -v149
	v_fma_f32 v150, v29, v58, -v150
	v_fma_f32 v151, v25, v59, -v151
	v_mul_f32_e64 v152, v25, v96
	v_fma_f32 v152, v29, v97, v152
	v_fma_f32 v152, v58, v148, v152
	v_rcp_f32_e32 v152, v152
	v_cmp_ne_u32_e64 vcc, s37, v3
	v_mul_f32_e64 v152, v152, v22
	v_cndmask_b32_e64 v152, 0, v152, s[30:31]
	v_cndmask_b32_e64 v25, 0, v18, vcc
	v_cndmask_b32_e64 v145, 0, v22, s[30:31]
	v_mul_f32_e64 v139, v96, v152
	v_mul_f32_e64 v140, v97, v152
	v_mul_f32_e64 v141, v148, v152
	v_mul_f32_e64 v142, v149, v152
	v_mul_f32_e64 v143, v150, v152
	v_mul_f32_e64 v144, v151, v152
	v_add_f32_e64 v146, v57, v25
	v_mov_b32_e32 v147, v3
	ds_write_b128 v23, v[136:139] offset:3072
	ds_write_b128 v23, v[140:143] offset:4096
	ds_write_b128 v23, v[144:147] offset:5120
	v_mov_b32_dpp v44, v46 wave_shr:1 row_mask:0xf bank_mask:0xf bound_ctrl:1
	v_mov_b32_dpp v45, v47 wave_shr:1 row_mask:0xf bank_mask:0xf bound_ctrl:1
	v_mov_b32_dpp v54, v46 wave_shl:1 row_mask:0xf bank_mask:0xf bound_ctrl:1
	v_mov_b32_dpp v55, v47 wave_shl:1 row_mask:0xf bank_mask:0xf bound_ctrl:1
	v_pk_mul_f32 v[56:57], v[46:47], v[68:69] op_sel_hi:[1,0]
	v_pk_mul_f32 v[58:59], v[46:47], v[68:69] op_sel:[0,1]
	v_pk_mul_f32 v[80:81], v[46:47], v[70:71] op_sel_hi:[1,0]
	v_pk_add_f32 v[82:83], v[46:47], v[44:45]
	v_pk_fma_f32 v[56:57], v[44:45], v[36:37], v[56:57] op_sel_hi:[1,0,1]
	v_pk_fma_f32 v[58:59], v[44:45], v[36:37], v[58:59] op_sel:[0,1,0]
	v_pk_fma_f32 v[80:81], v[44:45], v[38:39], v[80:81] op_sel_hi:[1,0,1]
	v_pk_add_f32 v[82:83], v[82:83], v[54:55]
	v_pk_fma_f32 v[56:57], v[54:55], v[40:41], v[56:57] op_sel_hi:[1,0,1]
	v_pk_fma_f32 v[58:59], v[54:55], v[40:41], v[58:59] op_sel:[0,1,0]
	v_pk_fma_f32 v[80:81], v[54:55], v[42:43], v[80:81] op_sel_hi:[1,0,1]
	s_waitcnt lgkmcnt(0)
	s_barrier
	v_pk_add_f32 v[44:45], v[60:61], v[82:83]
	v_pk_add_f32 v[54:55], v[66:67], v[56:57]
	v_pk_add_f32 v[60:61], v[50:51], v[58:59]
	v_pk_add_f32 v[50:51], v[62:63], v[80:81]
	v_pk_fma_f32 v[54:55], v[136:137], v[44:45], v[54:55] op_sel_hi:[0,1,1] neg_lo:[1,0,0] neg_hi:[1,0,0]
	v_pk_fma_f32 v[60:61], v[136:137], v[44:45], v[60:61] op_sel:[1,0,0] neg_lo:[1,0,0] neg_hi:[1,0,0]
	v_pk_fma_f32 v[50:51], v[138:139], v[44:45], v[50:51] op_sel_hi:[0,1,1] neg_lo:[1,0,0] neg_hi:[1,0,0]
	v_pk_mul_f32 v[62:63], v[138:139], v[54:55] op_sel:[1,0]
	v_pk_mul_f32 v[66:67], v[140:141], v[54:55] op_sel_hi:[0,1]
	v_pk_mul_f32 v[86:87], v[140:141], v[54:55] op_sel:[1,0]
	v_pk_fma_f32 v[62:63], v[140:141], v[60:61], v[62:63] op_sel_hi:[0,1,1]
	v_pk_fma_f32 v[66:67], v[142:143], v[60:61], v[66:67] op_sel_hi:[0,1,1]
	v_pk_fma_f32 v[86:87], v[142:143], v[60:61], v[86:87] op_sel:[1,0,0]
	v_pk_fma_f32 v[62:63], v[140:141], v[50:51], v[62:63] op_sel:[1,0,0]
	v_pk_fma_f32 v[66:67], v[142:143], v[50:51], v[66:67] op_sel:[1,0,0]
	v_pk_fma_f32 v[86:87], v[144:145], v[50:51], v[86:87] op_sel_hi:[0,1,1]
	v_pk_mul_f32 v[96:97], v[136:137], v[62:63] op_sel_hi:[0,1]
	v_pk_fma_f32 v[96:97], v[136:137], v[66:67], v[96:97] op_sel:[1,0,0]
	v_pk_fma_f32 v[96:97], v[138:139], v[86:87], v[96:97] op_sel_hi:[0,1,1]
	v_pk_fma_f32 v[96:97], v[144:145], v[44:45], v[96:97] op_sel:[1,0,0] neg_lo:[0,0,1] neg_hi:[0,0,1]
	s_add_i32 s5, s34, 4
	s_min_i32 s5, s5, 0x200
	s_mul_i32 s6, s5, 0x804
	s_add_i32 s6, s6, s35
	s_add_i32 s7, s6, 0x505014
	s_add_i32 s8, s6, 0x606018
	s_mul_i32 s9, s5, 0x180c
	s_add_i32 s9, s9, s33
	s_add_i32 s4, s34, 5
	s_min_i32 s4, s4, 0x200
	s_mul_i32 s4, s4, 0x804
	s_add_i32 s4, s4, s38
	buffer_load_dword v3, v28, s[20:23], s4 offen nt
	buffer_load_dwordx3 v[12:14], v27, s[24:27], s9 offen nt
	buffer_load_dword v6, v28, s[16:19], s7 offen nt
	buffer_load_dword v7, v28, s[16:19], s8 offen nt
	s_waitcnt vmcnt(8)
	v_mov_b32_dpp v72, v104 wave_shr:1 row_mask:0xf bank_mask:0xf bound_ctrl:1
	v_mov_b32_dpp v73, v105 wave_shr:1 row_mask:0xf bank_mask:0xf bound_ctrl:1
	v_mov_b32_dpp v74, v106 wave_shr:1 row_mask:0xf bank_mask:0xf bound_ctrl:1
	v_mov_b32_dpp v76, v104 wave_shl:1 row_mask:0xf bank_mask:0xf bound_ctrl:1
	v_mov_b32_dpp v77, v105 wave_shl:1 row_mask:0xf bank_mask:0xf bound_ctrl:1
	v_mov_b32_dpp v78, v106 wave_shl:1 row_mask:0xf bank_mask:0xf bound_ctrl:1
	s_add_i32 s4, s34, 3
	s_cmpk_lt_u32 s4, 0x201
	s_cselect_b64 s[12:13], s[40:41], 0
	v_cmp_eq_u32_e64 s[14:15], s37, v17
	s_and_b64 s[14:15], s[14:15], s[12:13]
	v_cndmask_b32_e64 v25, 0, 1, s[14:15]
	v_mul_f32_e64 v44, v104, v104
	v_mul_f32_e64 v45, v104, v105
	v_mul_f32_e64 v50, v104, v106
	v_mul_f32_e64 v51, v105, v105
	v_mul_f32_e64 v54, v105, v106
	v_mul_f32_e64 v55, v106, v106
	v_or_b32_dpp v29, v25, v25 wave_shr:1 row_mask:0xf bank_mask:0xf bound_ctrl:1
	s_nop 1
	v_or_b32_dpp v29, v25, v29 wave_shl:1 row_mask:0xf bank_mask:0xf bound_ctrl:1
	s_nop 1
	v_or_b32_dpp v30, v29, v29 wave_shr:1 row_mask:0xf bank_mask:0xf bound_ctrl:1
	s_nop 1
	v_or_b32_dpp v30, v29, v30 wave_shl:1 row_mask:0xf bank_mask:0xf bound_ctrl:1
	v_or3_b32 v25, v30, v53, v84
	v_or3_b32 v25, v25, v85, v52
	s_add_i32 s4, s34, 0
	s_cmpk_lt_u32 s4, 0x1ff
	s_cselect_b64 s[12:13], s[42:43], 0
	v_cmp_ne_u32_e64 s[30:31], 0, v25
	s_and_b64 s[30:31], s[30:31], s[12:13]
	v_cndmask_b32_e64 v25, 0, 1.0, s[30:31]
	v_add_f32_e64 v60, v104, v72
	v_add_f32_e64 v61, v105, v73
	v_add_f32_e64 v136, v106, v74
	v_fma_f32 v44, v72, v72, v44
	v_fma_f32 v45, v72, v73, v45
	v_fma_f32 v50, v72, v74, v50
	v_fma_f32 v51, v73, v73, v51
	v_fma_f32 v54, v73, v74, v54
	v_fma_f32 v55, v74, v74, v55
	v_add_f32_dpp v143, v25, v25 wave_shr:1 row_mask:0xf bank_mask:0xf bound_ctrl:1
	v_add_f32_e64 v60, v60, v76
	v_add_f32_e64 v61, v61, v77
	v_add_f32_e64 v136, v136, v78
	v_fma_f32 v137, v76, v76, v44
	v_fma_f32 v138, v76, v77, v45
	v_fma_f32 v139, v76, v78, v50
	v_fma_f32 v140, v77, v77, v51
	v_fma_f32 v141, v77, v78, v54
	v_fma_f32 v142, v78, v78, v55
	v_add_f32_dpp v143, v25, v143 wave_shl:1 row_mask:0xf bank_mask:0xf bound_ctrl:1
	v_pk_add_f32 v[44:45], v[100:101], v[60:61]
	v_pk_add_f32 v[50:51], v[118:119], v[44:45]
	v_pk_add_f32 v[54:55], v[128:129], v[136:137]
	v_pk_add_f32 v[100:101], v[120:121], v[54:55]
	v_pk_add_f32 v[118:119], v[130:131], v[138:139]
	v_pk_add_f32 v[120:121], v[122:123], v[118:119]
	v_pk_add_f32 v[122:123], v[132:133], v[140:141]
	v_pk_add_f32 v[128:129], v[124:125], v[122:123]
	v_pk_add_f32 v[124:125], v[134:135], v[142:143]
	v_pk_add_f32 v[130:131], v[126:127], v[124:125]
	v_mul_f32_e64 v132, v50, v22
	v_mul_f32_e64 v133, v51, v22
	v_mul_f32_e64 v134, v100, v22
	v_fma_f32 v25, v101, v22, v26
	v_mul_f32_e64 v29, v120, v22
	v_mul_f32_e64 v126, v121, v22
	v_fma_f32 v127, v128, v22, v26
	v_mul_f32_e64 v152, v129, v22
	v_fma_f32 v153, v130, v22, v26
	v_fma_f32 v25, -v132, v132, v25
	v_fma_f32 v29, -v132, v133, v29
	v_fma_f32 v126, -v132, v134, v126
	v_fma_f32 v127, -v133, v133, v127
	v_fma_f32 v152, -v133, v134, v152
	v_fma_f32 v153, -v134, v134, v153
	v_mul_f32_e64 v154, v152, v152
	v_mul_f32_e64 v155, v29, v153
	v_mul_f32_e64 v156, v126, v127
	v_mul_f32_e64 v157, v126, v126
	v_mul_f32_e64 v158, v25, v152
	v_mul_f32_e64 v159, v29, v29
	v_fma_f32 v154, v127, v153, -v154
	v_fma_f32 v155, v126, v152, -v155
	v_fma_f32 v156, v29, v152, -v156
	v_fma_f32 v157, v25, v153, -v157
	v_fma_f32 v158, v29, v126, -v158
	v_fma_f32 v159, v25, v127, -v159
	v_mul_f32_e64 v160, v25, v154
	v_fma_f32 v160, v29, v155, v160
	v_fma_f32 v160, v126, v156, v160
	v_rcp_f32_e32 v160, v160
	v_cmp_ne_u32_e64 vcc, s37, v16
	v_mul_f32_e64 v160, v160, v22
	v_cndmask_b32_e64 v160, 0, v160, s[30:31]
	v_cndmask_b32_e64 v25, 0, v18, vcc
	v_cndmask_b32_e64 v149, 0, v22, s[30:31]
	v_mul_f32_e64 v135, v154, v160
	v_mul_f32_e64 v144, v155, v160
	v_mul_f32_e64 v145, v156, v160
	v_mul_f32_e64 v146, v157, v160
	v_mul_f32_e64 v147, v158, v160
	v_mul_f32_e64 v148, v159, v160
	v_add_f32_e64 v150, v131, v25
	v_mov_b32_e32 v151, v16
	ds_write_b128 v23, v[132:135]
	ds_write_b128 v23, v[144:147] offset:1024
	ds_write_b128 v23, v[148:151] offset:2048
	v_mov_b32_dpp v50, v48 wave_shr:1 row_mask:0xf bank_mask:0xf bound_ctrl:1
	v_mov_b32_dpp v51, v49 wave_shr:1 row_mask:0xf bank_mask:0xf bound_ctrl:1
	v_mov_b32_dpp v100, v48 wave_shl:1 row_mask:0xf bank_mask:0xf bound_ctrl:1
	v_mov_b32_dpp v101, v49 wave_shl:1 row_mask:0xf bank_mask:0xf bound_ctrl:1
	v_pk_mul_f32 v[120:121], v[48:49], v[104:105] op_sel_hi:[1,0]
	v_pk_mul_f32 v[126:127], v[48:49], v[104:105] op_sel:[0,1]
	v_pk_mul_f32 v[128:129], v[48:49], v[106:107] op_sel_hi:[1,0]
	v_pk_add_f32 v[130:131], v[48:49], v[50:51]
	v_pk_fma_f32 v[120:121], v[50:51], v[72:73], v[120:121] op_sel_hi:[1,0,1]
	v_pk_fma_f32 v[126:127], v[50:51], v[72:73], v[126:127] op_sel:[0,1,0]
	v_pk_fma_f32 v[128:129], v[50:51], v[74:75], v[128:129] op_sel_hi:[1,0,1]
	v_pk_add_f32 v[130:131], v[130:131], v[100:101]
	v_pk_fma_f32 v[120:121], v[100:101], v[76:77], v[120:121] op_sel_hi:[1,0,1]
	v_pk_fma_f32 v[126:127], v[100:101], v[76:77], v[126:127] op_sel:[0,1,0]
	v_pk_fma_f32 v[128:129], v[100:101], v[78:79], v[128:129] op_sel_hi:[1,0,1]
	s_waitcnt lgkmcnt(0)
	s_barrier
	v_pk_add_f32 v[50:51], v[82:83], v[130:131]
	v_pk_add_f32 v[100:101], v[94:95], v[50:51]
	v_pk_add_f32 v[82:83], v[56:57], v[120:121]
	v_pk_add_f32 v[94:95], v[88:89], v[82:83]
	v_pk_add_f32 v[56:57], v[58:59], v[126:127]
	v_pk_add_f32 v[88:89], v[90:91], v[56:57]
	v_pk_add_f32 v[58:59], v[80:81], v[128:129]
	v_pk_add_f32 v[90:91], v[92:93], v[58:59]
	v_pk_fma_f32 v[94:95], v[132:133], v[100:101], v[94:95] op_sel_hi:[0,1,1] neg_lo:[1,0,0] neg_hi:[1,0,0]
	v_pk_fma_f32 v[88:89], v[132:133], v[100:101], v[88:89] op_sel:[1,0,0] neg_lo:[1,0,0] neg_hi:[1,0,0]
	v_pk_fma_f32 v[90:91], v[134:135], v[100:101], v[90:91] op_sel_hi:[0,1,1] neg_lo:[1,0,0] neg_hi:[1,0,0]
	v_pk_mul_f32 v[80:81], v[134:135], v[94:95] op_sel:[1,0]
	v_pk_mul_f32 v[92:93], v[144:145], v[94:95] op_sel_hi:[0,1]
	v_pk_mul_f32 v[152:153], v[144:145], v[94:95] op_sel:[1,0]
	v_pk_fma_f32 v[80:81], v[144:145], v[88:89], v[80:81] op_sel_hi:[0,1,1]
	v_pk_fma_f32 v[92:93], v[146:147], v[88:89], v[92:93] op_sel_hi:[0,1,1]
	v_pk_fma_f32 v[152:153], v[146:147], v[88:89], v[152:153] op_sel:[1,0,0]
	v_pk_fma_f32 v[80:81], v[144:145], v[90:91], v[80:81] op_sel:[1,0,0]
	v_pk_fma_f32 v[92:93], v[146:147], v[90:91], v[92:93] op_sel:[1,0,0]
	v_pk_fma_f32 v[152:153], v[148:149], v[90:91], v[152:153] op_sel_hi:[0,1,1]
	v_pk_mul_f32 v[154:155], v[132:133], v[80:81] op_sel_hi:[0,1]
	v_pk_fma_f32 v[154:155], v[132:133], v[92:93], v[154:155] op_sel:[1,0,0]
	v_pk_fma_f32 v[154:155], v[134:135], v[152:153], v[154:155] op_sel_hi:[0,1,1]
	v_pk_fma_f32 v[154:155], v[148:149], v[100:101], v[154:155] op_sel:[1,0,0] neg_lo:[0,0,1] neg_hi:[0,0,1]
	v_cmp_eq_u32_e64 s[10:11], 6, v151
	v_cmp_eq_u32_e64 s[14:15], 7, v151
	v_pk_add_f32 v[88:89], v[62:63], v[80:81]
	v_pk_add_f32 v[90:91], v[64:65], v[88:89]
	v_pk_add_f32 v[62:63], v[66:67], v[92:93]
	v_pk_add_f32 v[64:65], v[98:99], v[62:63]
	v_pk_add_f32 v[66:67], v[86:87], v[152:153]
	v_pk_add_f32 v[94:95], v[102:103], v[66:67]
	v_pk_add_f32 v[86:87], v[96:97], v[154:155]
	v_pk_add_f32 v[98:99], v[116:117], v[86:87]
	v_pk_fma_f32 v[96:97], v[108:109], v[90:91], v[98:99] op_sel_hi:[0,1,1]
	v_pk_fma_f32 v[100:101], v[112:113], v[90:91], v[98:99] op_sel_hi:[0,1,1]
	v_pk_fma_f32 v[96:97], v[108:109], v[64:65], v[96:97] op_sel:[1,0,0]
	v_pk_fma_f32 v[100:101], v[112:113], v[64:65], v[100:101] op_sel:[1,0,0]
	v_pk_fma_f32 v[96:97], v[110:111], v[94:95], v[96:97] op_sel_hi:[0,1,1]
	v_pk_fma_f32 v[100:101], v[114:115], v[94:95], v[100:101] op_sel_hi:[0,1,1]
	v_pk_fma_f32 v[98:99], v[32:33], v[90:91], v[98:99] op_sel_hi:[0,1,1]
	v_pk_fma_f32 v[98:99], v[32:33], v[64:65], v[98:99] op_sel:[1,0,0]
	v_pk_fma_f32 v[98:99], v[34:35], v[94:95], v[98:99] op_sel_hi:[0,1,1]
	v_cndmask_b32_e64 v102, 0, v18, s[10:11]
	v_cndmask_b32_e64 v103, 0, v18, s[14:15]
	v_add_f32_dpp v98, v96, v98 wave_shl:1 row_mask:0xf bank_mask:0xf bound_ctrl:1
	v_add_f32_dpp v99, v97, v99 wave_shl:1 row_mask:0xf bank_mask:0xf bound_ctrl:1
	s_add_i32 s4, s34, 0
	s_cmpk_lt_i32 s4, 0x201
	s_cselect_b64 s[12:13], s[0:1], 0
	v_add_f32_dpp v98, v100, v98 wave_shr:1 row_mask:0xf bank_mask:0xf bound_ctrl:1
	v_add_f32_dpp v99, v101, v99 wave_shr:1 row_mask:0xf bank_mask:0xf bound_ctrl:1
	v_pk_fma_f32 v[98:99], v[20:21], v[150:151], v[98:99] op_sel_hi:[1,0,1] neg_lo:[0,0,1] neg_hi:[0,0,1]
	v_pk_add_f32 v[98:99], v[98:99], v[102:103] neg_lo:[0,1] neg_hi:[0,1]
	v_pk_mul_f32 v[116:117], v[98:99], v[98:99]
	v_add_f32_e32 v116, v116, v117
	v_cndmask_b32_e64 v117, 0, v116, s[12:13]
	v_add_f32_e32 v1, v1, v117
	s_add_i32 s5, s34, 5
	s_min_i32 s5, s5, 0x200
	s_mul_i32 s6, s5, 0x804
	s_add_i32 s6, s6, s35
	s_add_i32 s7, s6, 0x505014
	s_add_i32 s8, s6, 0x606018
	s_mul_i32 s9, s5, 0x180c
	s_add_i32 s9, s9, s33
	s_add_i32 s4, s34, 6
	s_min_i32 s4, s4, 0x200
	s_mul_i32 s4, s4, 0x804
	s_add_i32 s4, s4, s38
	buffer_load_dword v16, v28, s[20:23], s4 offen nt
	buffer_load_dwordx3 v[32:34], v27, s[24:27], s9 offen nt
	buffer_load_dword v20, v28, s[16:19], s7 offen nt
	buffer_load_dword v21, v28, s[16:19], s8 offen nt
	s_waitcnt vmcnt(8)
	v_mov_b32_dpp v96, v8 wave_shr:1 row_mask:0xf bank_mask:0xf bound_ctrl:1
	v_mov_b32_dpp v97, v9 wave_shr:1 row_mask:0xf bank_mask:0xf bound_ctrl:1
	v_mov_b32_dpp v98, v10 wave_shr:1 row_mask:0xf bank_mask:0xf bound_ctrl:1
	v_mov_b32_dpp v100, v8 wave_shl:1 row_mask:0xf bank_mask:0xf bound_ctrl:1
	v_mov_b32_dpp v101, v9 wave_shl:1 row_mask:0xf bank_mask:0xf bound_ctrl:1
	v_mov_b32_dpp v102, v10 wave_shl:1 row_mask:0xf bank_mask:0xf bound_ctrl:1
	s_add_i32 s4, s34, 4
	s_cmpk_lt_u32 s4, 0x201
	s_cselect_b64 s[12:13], s[40:41], 0
	v_cmp_eq_u32_e64 s[14:15], s37, v2
	s_and_b64 s[14:15], s[14:15], s[12:13]
	v_cndmask_b32_e64 v25, 0, 1, s[14:15]
	v_mul_f32_e64 v64, v8, v8
	v_mul_f32_e64 v65, v8, v9
	v_mul_f32_e64 v90, v8, v10
	v_mul_f32_e64 v91, v9, v9
	v_mul_f32_e64 v94, v9, v10
	v_mul_f32_e64 v95, v10, v10
	v_or_b32_dpp v29, v25, v25 wave_shr:1 row_mask:0xf bank_mask:0xf bound_ctrl:1
	s_nop 1
	v_or_b32_dpp v29, v25, v29 wave_shl:1 row_mask:0xf bank_mask:0xf bound_ctrl:1
	s_nop 1
	v_or_b32_dpp v52, v29, v29 wave_shr:1 row_mask:0xf bank_mask:0xf bound_ctrl:1
	s_nop 1
	v_or_b32_dpp v52, v29, v52 wave_shl:1 row_mask:0xf bank_mask:0xf bound_ctrl:1
	v_or3_b32 v25, v52, v30, v53
	v_or3_b32 v25, v25, v84, v85
	s_add_i32 s4, s34, 1
	s_cmpk_lt_u32 s4, 0x1ff
	s_cselect_b64 s[12:13], s[42:43], 0
	v_cmp_ne_u32_e64 s[30:31], 0, v25
	s_and_b64 s[30:31], s[30:31], s[12:13]
	v_cndmask_b32_e64 v25, 0, 1.0, s[30:31]
	v_add_f32_e64 v108, v8, v96
	v_add_f32_e64 v109, v9, v97
	v_add_f32_e64 v110, v10, v98
	v_fma_f32 v64, v96, v96, v64
	v_fma_f32 v65, v96, v97, v65
	v_fma_f32 v90, v96, v98, v90
	v_fma_f32 v91, v97, v97, v91
	v_fma_f32 v94, v97, v98, v94
	v_fma_f32 v95, v98, v98, v95
	v_add_f32_dpp v117, v25, v25 wave_shr:1 row_mask:0xf bank_mask:0xf bound_ctrl:1
	v_add_f32_e64 v108, v108, v100
	v_add_f32_e64 v109, v109, v101
	v_add_f32_e64 v110, v110, v102
	v_fma_f32 v111, v100, v100, v64
	v_fma_f32 v112, v100, v101, v65
	v_fma_f32 v113, v100, v102, v90
	v_fma_f32 v114, v101, v101, v91
	v_fma_f32 v115, v101, v102, v94
	v_fma_f32 v116, v102, v102, v95
	v_add_f32_dpp v117, v25, v117 wave_shl:1 row_mask:0xf bank_mask:0xf bound_ctrl:1
	v_pk_add_f32 v[64:65], v[44:45], v[108:109]
	v_pk_add_f32 v[44:45], v[54:55], v[110:111]
	v_pk_add_f32 v[54:55], v[118:119], v[112:113]
	v_pk_add_f32 v[90:91], v[122:123], v[114:115]
	v_pk_add_f32 v[94:95], v[124:125], v[116:117]
	v_mul_f32_e64 v132, v64, v22
	v_mul_f32_e64 v133, v65, v22
	v_mul_f32_e64 v134, v44, v22
	v_fma_f32 v25, v45, v22, v26
	v_mul_f32_e64 v29, v54, v22
	v_mul_f32_e64 v118, v55, v22
	v_fma_f32 v119, v90, v22, v26
	v_mul_f32_e64 v122, v91, v22
	v_fma_f32 v123, v94, v22, v26
	v_fma_f32 v25, -v132, v132, v25
	v_fma_f32 v29, -v132, v133, v29
	v_fma_f32 v118, -v132, v134, v118
	v_fma_f32 v119, -v133, v133, v119
	v_fma_f32 v122, -v133, v134, v122
	v_fma_f32 v123, -v134, v134, v123
	v_mul_f32_e64 v124, v122, v122
	v_mul_f32_e64 v125, v29, v123
	v_mul_f32_e64 v156, v118, v119
	v_mul_f32_e64 v157, v118, v118
	v_mul_f32_e64 v158, v25, v122
	v_mul_f32_e64 v159, v29, v29
	v_fma_f32 v124, v119, v123, -v124
	v_fma_f32 v125, v118, v122, -v125
	v_fma_f32 v156, v29, v122, -v156
	v_fma_f32 v157, v25, v123, -v157
	v_fma_f32 v158, v29, v118, -v158
	v_fma_f32 v159, v25, v119, -v159
	v_mul_f32_e64 v160, v25, v124
	v_fma_f32 v160, v29, v125, v160
	v_fma_f32 v160, v118, v156, v160
	v_rcp_f32_e32 v160, v160
	v_cmp_ne_u32_e64 vcc, s37, v31
	v_mul_f32_e64 v160, v160, v22
	v_cndmask_b32_e64 v160, 0, v160, s[30:31]
	v_cndmask_b32_e64 v25, 0, v18, vcc
	v_cndmask_b32_e64 v149, 0, v22, s[30:31]
	v_mul_f32_e64 v135, v124, v160
	v_mul_f32_e64 v144, v125, v160
	v_mul_f32_e64 v145, v156, v160
	v_mul_f32_e64 v146, v157, v160
	v_mul_f32_e64 v147, v158, v160
	v_mul_f32_e64 v148, v159, v160
	v_add_f32_e64 v150, v95, v25
	v_mov_b32_e32 v151, v31
	ds_write_b128 v23, v[132:135] offset:3072
	ds_write_b128 v23, v[144:147] offset:4096
	ds_write_b128 v23, v[148:151] offset:5120
	v_mov_b32_dpp v44, v4 wave_shr:1 row_mask:0xf bank_mask:0xf bound_ctrl:1
	v_mov_b32_dpp v45, v5 wave_shr:1 row_mask:0xf bank_mask:0xf bound_ctrl:1
	v_mov_b32_dpp v54, v4 wave_shl:1 row_mask:0xf bank_mask:0xf bound_ctrl:1
	v_mov_b32_dpp v55, v5 wave_shl:1 row_mask:0xf bank_mask:0xf bound_ctrl:1
	v_pk_mul_f32 v[64:65], v[4:5], v[8:9] op_sel_hi:[1,0]
	v_pk_mul_f32 v[90:91], v[4:5], v[8:9] op_sel:[0,1]
	v_pk_mul_f32 v[94:95], v[4:5], v[10:11] op_sel_hi:[1,0]
	v_pk_add_f32 v[118:119], v[4:5], v[44:45]
	v_pk_fma_f32 v[64:65], v[44:45], v[96:97], v[64:65] op_sel_hi:[1,0,1]
	v_pk_fma_f32 v[90:91], v[44:45], v[96:97], v[90:91] op_sel:[0,1,0]
	v_pk_fma_f32 v[94:95], v[44:45], v[98:99], v[94:95] op_sel_hi:[1,0,1]
	v_pk_add_f32 v[118:119], v[118:119], v[54:55]
	v_pk_fma_f32 v[64:65], v[54:55], v[100:101], v[64:65] op_sel_hi:[1,0,1]
	v_pk_fma_f32 v[90:91], v[54:55], v[100:101], v[90:91] op_sel:[0,1,0]
	v_pk_fma_f32 v[94:95], v[54:55], v[102:103], v[94:95] op_sel_hi:[1,0,1]
	s_waitcnt lgkmcnt(0)
	s_barrier
	v_pk_add_f32 v[44:45], v[50:51], v[118:119]
	v_pk_add_f32 v[50:51], v[82:83], v[64:65]
	v_pk_add_f32 v[54:55], v[56:57], v[90:91]
	v_pk_add_f32 v[56:57], v[58:59], v[94:95]
	v_pk_fma_f32 v[50:51], v[132:133], v[44:45], v[50:51] op_sel_hi:[0,1,1] neg_lo:[1,0,0] neg_hi:[1,0,0]
	v_pk_fma_f32 v[54:55], v[132:133], v[44:45], v[54:55] op_sel:[1,0,0] neg_lo:[1,0,0] neg_hi:[1,0,0]
	v_pk_fma_f32 v[56:57], v[134:135], v[44:45], v[56:57] op_sel_hi:[0,1,1] neg_lo:[1,0,0] neg_hi:[1,0,0]
	v_pk_mul_f32 v[58:59], v[134:135], v[50:51] op_sel:[1,0]
	v_pk_mul_f32 v[82:83], v[144:145], v[50:51] op_sel_hi:[0,1]
	v_pk_mul_f32 v[122:123], v[144:145], v[50:51] op_sel:[1,0]
	v_pk_fma_f32 v[58:59], v[144:145], v[54:55], v[58:59] op_sel_hi:[0,1,1]
	v_pk_fma_f32 v[82:83], v[146:147], v[54:55], v[82:83] op_sel_hi:[0,1,1]
	v_pk_fma_f32 v[122:123], v[146:147], v[54:55], v[122:123] op_sel:[1,0,0]
	v_pk_fma_f32 v[58:59], v[144:145], v[56:57], v[58:59] op_sel:[1,0,0]
	v_pk_fma_f32 v[82:83], v[146:147], v[56:57], v[82:83] op_sel:[1,0,0]
	v_pk_fma_f32 v[122:123], v[148:149], v[56:57], v[122:123] op_sel_hi:[0,1,1]
	v_pk_mul_f32 v[124:125], v[132:133], v[58:59] op_sel_hi:[0,1]
	v_pk_fma_f32 v[124:125], v[132:133], v[82:83], v[124:125] op_sel:[1,0,0]
	v_pk_fma_f32 v[124:125], v[134:135], v[122:123], v[124:125] op_sel_hi:[0,1,1]
	v_pk_fma_f32 v[124:125], v[148:149], v[44:45], v[124:125] op_sel:[1,0,0] neg_lo:[0,0,1] neg_hi:[0,0,1]
	v_cmp_eq_u32_e64 s[10:11], 6, v151
	v_cmp_eq_u32_e64 s[14:15], 7, v151
	v_pk_add_f32 v[44:45], v[88:89], v[58:59]
	v_pk_add_f32 v[50:51], v[62:63], v[82:83]
	v_pk_add_f32 v[54:55], v[66:67], v[122:123]
	v_pk_add_f32 v[56:57], v[86:87], v[124:125]
	v_pk_fma_f32 v[62:63], v[36:37], v[44:45], v[56:57] op_sel_hi:[0,1,1]
	v_pk_fma_f32 v[66:67], v[40:41], v[44:45], v[56:57] op_sel_hi:[0,1,1]
	v_pk_fma_f32 v[62:63], v[36:37], v[50:51], v[62:63] op_sel:[1,0,0]
	v_pk_fma_f32 v[66:67], v[40:41], v[50:51], v[66:67] op_sel:[1,0,0]
	v_pk_fma_f32 v[62:63], v[38:39], v[54:55], v[62:63] op_sel_hi:[0,1,1]
	v_pk_fma_f32 v[66:67], v[42:43], v[54:55], v[66:67] op_sel_hi:[0,1,1]
	v_pk_fma_f32 v[56:57], v[68:69], v[44:45], v[56:57] op_sel_hi:[0,1,1]
	v_pk_fma_f32 v[56:57], v[68:69], v[50:51], v[56:57] op_sel:[1,0,0]
	v_pk_fma_f32 v[56:57], v[70:71], v[54:55], v[56:57] op_sel_hi:[0,1,1]
	v_cndmask_b32_e64 v86, 0, v18, s[10:11]
	v_cndmask_b32_e64 v87, 0, v18, s[14:15]
	v_add_f32_dpp v56, v62, v56 wave_shl:1 row_mask:0xf bank_mask:0xf bound_ctrl:1
	v_add_f32_dpp v57, v63, v57 wave_shl:1 row_mask:0xf bank_mask:0xf bound_ctrl:1
	s_add_i32 s4, s34, 1
	s_cmpk_lt_i32 s4, 0x201
	s_cselect_b64 s[12:13], s[0:1], 0
	v_add_f32_dpp v56, v66, v56 wave_shr:1 row_mask:0xf bank_mask:0xf bound_ctrl:1
	v_add_f32_dpp v57, v67, v57 wave_shr:1 row_mask:0xf bank_mask:0xf bound_ctrl:1
	v_pk_fma_f32 v[56:57], v[46:47], v[150:151], v[56:57] op_sel_hi:[1,0,1] neg_lo:[0,0,1] neg_hi:[0,0,1]
	v_pk_add_f32 v[56:57], v[56:57], v[86:87] neg_lo:[0,1] neg_hi:[0,1]
	v_pk_mul_f32 v[88:89], v[56:57], v[56:57]
	v_add_f32_e32 v88, v88, v89
	v_cndmask_b32_e64 v89, 0, v88, s[12:13]
	v_add_f32_e32 v1, v1, v89
	s_add_i32 s5, s34, 6
	s_min_i32 s5, s5, 0x200
	s_mul_i32 s6, s5, 0x804
	s_add_i32 s6, s6, s35
	s_add_i32 s7, s6, 0x505014
	s_add_i32 s8, s6, 0x606018
	s_mul_i32 s9, s5, 0x180c
	s_add_i32 s9, s9, s33
	s_add_i32 s4, s34, 7
	s_min_i32 s4, s4, 0x200
	s_mul_i32 s4, s4, 0x804
	s_add_i32 s4, s4, s38
	buffer_load_dword v25, v28, s[20:23], s4 offen nt
	buffer_load_dwordx3 v[40:42], v27, s[24:27], s9 offen nt
	buffer_load_dword v36, v28, s[16:19], s7 offen nt
	buffer_load_dword v37, v28, s[16:19], s8 offen nt
	s_waitcnt vmcnt(8)
	v_mov_b32_dpp v44, v12 wave_shr:1 row_mask:0xf bank_mask:0xf bound_ctrl:1
	v_mov_b32_dpp v45, v13 wave_shr:1 row_mask:0xf bank_mask:0xf bound_ctrl:1
	v_mov_b32_dpp v46, v14 wave_shr:1 row_mask:0xf bank_mask:0xf bound_ctrl:1
	v_mov_b32_dpp v68, v12 wave_shl:1 row_mask:0xf bank_mask:0xf bound_ctrl:1
	v_mov_b32_dpp v69, v13 wave_shl:1 row_mask:0xf bank_mask:0xf bound_ctrl:1
	v_mov_b32_dpp v70, v14 wave_shl:1 row_mask:0xf bank_mask:0xf bound_ctrl:1
	s_add_i32 s4, s34, 5
	s_cmpk_lt_u32 s4, 0x201
	s_cselect_b64 s[12:13], s[40:41], 0
	v_cmp_eq_u32_e64 s[14:15], s37, v3
	s_and_b64 s[14:15], s[14:15], s[12:13]
	v_cndmask_b32_e64 v29, 0, 1, s[14:15]
	v_mul_f32_e64 v38, v12, v12
	v_mul_f32_e64 v39, v12, v13
	v_mul_f32_e64 v50, v12, v14
	v_mul_f32_e64 v51, v13, v13
	v_mul_f32_e64 v54, v13, v14
	v_mul_f32_e64 v55, v14, v14
	v_or_b32_dpp v31, v29, v29 wave_shr:1 row_mask:0xf bank_mask:0xf bound_ctrl:1
	s_nop 1
	v_or_b32_dpp v31, v29, v31 wave_shl:1 row_mask:0xf bank_mask:0xf bound_ctrl:1
	s_nop 1
	v_or_b32_dpp v85, v31, v31 wave_shr:1 row_mask:0xf bank_mask:0xf bound_ctrl:1
	s_nop 1
	v_or_b32_dpp v85, v31, v85 wave_shl:1 row_mask:0xf bank_mask:0xf bound_ctrl:1
	v_or3_b32 v29, v85, v52, v30
	v_or3_b32 v29, v29, v53, v84
	s_add_i32 s4, s34, 2
	s_cmpk_lt_u32 s4, 0x1ff
	s_cselect_b64 s[12:13], s[42:43], 0
	v_cmp_ne_u32_e64 s[30:31], 0, v29
	s_and_b64 s[30:31], s[30:31], s[12:13]
	v_cndmask_b32_e64 v29, 0, 1.0, s[30:31]
	v_add_f32_e64 v56, v12, v44
	v_add_f32_e64 v57, v13, v45
	v_add_f32_e64 v62, v14, v46
	v_fma_f32 v38, v44, v44, v38
	v_fma_f32 v39, v44, v45, v39
	v_fma_f32 v50, v44, v46, v50
	v_fma_f32 v51, v45, v45, v51
	v_fma_f32 v54, v45, v46, v54
	v_fma_f32 v55, v46, v46, v55
	v_add_f32_dpp v89, v29, v29 wave_shr:1 row_mask:0xf bank_mask:0xf bound_ctrl:1
	v_add_f32_e64 v56, v56, v68
	v_add_f32_e64 v57, v57, v69
	v_add_f32_e64 v62, v62, v70
	v_fma_f32 v63, v68, v68, v38
	v_fma_f32 v66, v68, v69, v39
	v_fma_f32 v67, v68, v70, v50
	v_fma_f32 v86, v69, v69, v51
	v_fma_f32 v87, v69, v70, v54
	v_fma_f32 v88, v70, v70, v55
	v_add_f32_dpp v89, v29, v89 wave_shl:1 row_mask:0xf bank_mask:0xf bound_ctrl:1
	v_pk_add_f32 v[38:39], v[108:109], v[56:57]
	v_pk_add_f32 v[50:51], v[60:61], v[38:39]
	v_pk_add_f32 v[54:55], v[110:111], v[62:63]
	v_pk_add_f32 v[60:61], v[136:137], v[54:55]
	v_pk_add_f32 v[108:109], v[112:113], v[66:67]
	v_pk_add_f32 v[110:111], v[138:139], v[108:109]
	v_pk_add_f32 v[112:113], v[114:115], v[86:87]
	v_pk_add_f32 v[132:133], v[140:141], v[112:113]
	v_pk_add_f32 v[114:115], v[116:117], v[88:89]
	v_pk_add_f32 v[134:135], v[142:143], v[114:115]
	v_mul_f32_e64 v136, v50, v22
	v_mul_f32_e64 v137, v51, v22
	v_mul_f32_e64 v138, v60, v22
	v_fma_f32 v29, v61, v22, v26
	v_mul_f32_e64 v31, v110, v22
	v_mul_f32_e64 v116, v111, v22
	v_fma_f32 v117, v132, v22, v26
	v_mul_f32_e64 v148, v133, v22
	v_fma_f32 v149, v134, v22, v26
	v_fma_f32 v29, -v136, v136, v29
	v_fma_f32 v31, -v136, v137, v31
	v_fma_f32 v116, -v136, v138, v116
	v_fma_f32 v117, -v137, v137, v117
	v_fma_f32 v148, -v137, v138, v148
	v_fma_f32 v149, -v138, v138, v149
	v_mul_f32_e64 v150, v148, v148
	v_mul_f32_e64 v151, v31, v149
	v_mul_f32_e64 v156, v116, v117
	v_mul_f32_e64 v157, v116, v116
	v_mul_f32_e64 v158, v29, v148
	v_mul_f32_e64 v159, v31, v31
	v_fma_f32 v150, v117, v149, -v150
	v_fma_f32 v151, v116, v148, -v151
	v_fma_f32 v156, v31, v148, -v156
	v_fma_f32 v157, v29, v149, -v157
	v_fma_f32 v158, v31, v116, -v158
	v_fma_f32 v159, v29, v117, -v159
	v_mul_f32_e64 v160, v29, v150
	v_fma_f32 v160, v31, v151, v160
	v_fma_f32 v160, v116, v156, v160
	v_rcp_f32_e32 v160, v160
	v_cmp_ne_u32_e64 vcc, s37, v24
	v_mul_f32_e64 v160, v160, v22
	v_cndmask_b32_e64 v160, 0, v160, s[30:31]
	v_cndmask_b32_e64 v29, 0, v18, vcc
	v_cndmask_b32_e64 v145, 0, v22, s[30:31]
	v_mul_f32_e64 v139, v150, v160
	v_mul_f32_e64 v140, v151, v160
	v_mul_f32_e64 v141, v156, v160
	v_mul_f32_e64 v142, v157, v160
	v_mul_f32_e64 v143, v158, v160
	v_mul_f32_e64 v144, v159, v160
	v_add_f32_e64 v146, v135, v29
	v_mov_b32_e32 v147, v24
	ds_write_b128 v23, v[136:139]
	ds_write_b128 v23, v[140:143] offset:1024
	ds_write_b128 v23, v[144:147] offset:2048
	v_mov_b32_dpp v50, v6 wave_shr:1 row_mask:0xf bank_mask:0xf bound_ctrl:1
	v_mov_b32_dpp v51, v7 wave_shr:1 row_mask:0xf bank_mask:0xf bound_ctrl:1
	v_mov_b32_dpp v60, v6 wave_shl:1 row_mask:0xf bank_mask:0xf bound_ctrl:1
	v_mov_b32_dpp v61, v7 wave_shl:1 row_mask:0xf bank_mask:0xf bound_ctrl:1
	v_pk_mul_f32 v[110:111], v[6:7], v[12:13] op_sel_hi:[1,0]
	v_pk_mul_f32 v[116:117], v[6:7], v[12:13] op_sel:[0,1]
	v_pk_mul_f32 v[132:133], v[6:7], v[14:15] op_sel_hi:[1,0]
	v_pk_add_f32 v[134:135], v[6:7], v[50:51]
	v_pk_fma_f32 v[110:111], v[50:51], v[44:45], v[110:111] op_sel_hi:[1,0,1]
	v_pk_fma_f32 v[116:117], v[50:51], v[44:45], v[116:117] op_sel:[0,1,0]
	v_pk_fma_f32 v[132:133], v[50:51], v[46:47], v[132:133] op_sel_hi:[1,0,1]
	v_pk_add_f32 v[134:135], v[134:135], v[60:61]
	v_pk_fma_f32 v[110:111], v[60:61], v[68:69], v[110:111] op_sel_hi:[1,0,1]
	v_pk_fma_f32 v[116:117], v[60:61], v[68:69], v[116:117] op_sel:[0,1,0]
	v_pk_fma_f32 v[132:133], v[60:61], v[70:71], v[132:133] op_sel_hi:[1,0,1]
	s_waitcnt lgkmcnt(0)
	s_barrier
	v_pk_add_f32 v[50:51], v[118:119], v[134:135]
	v_pk_add_f32 v[60:61], v[130:131], v[50:51]
	v_pk_add_f32 v[118:119], v[64:65], v[110:111]
	v_pk_add_f32 v[130:131], v[120:121], v[118:119]
	v_pk_add_f32 v[64:65], v[90:91], v[116:117]
	v_pk_add_f32 v[120:121], v[126:127], v[64:65]
	v_pk_add_f32 v[90:91], v[94:95], v[132:133]
	v_pk_add_f32 v[126:127], v[128:129], v[90:91]
	v_pk_fma_f32 v[130:131], v[136:137], v[60:61], v[130:131] op_sel_hi:[0,1,1] neg_lo:[1,0,0] neg_hi:[1,0,0]
	v_pk_fma_f32 v[120:121], v[136:137], v[60:61], v[120:121] op_sel:[1,0,0] neg_lo:[1,0,0] neg_hi:[1,0,0]
	v_pk_fma_f32 v[126:127], v[138:139], v[60:61], v[126:127] op_sel_hi:[0,1,1] neg_lo:[1,0,0] neg_hi:[1,0,0]
	v_pk_mul_f32 v[94:95], v[138:139], v[130:131] op_sel:[1,0]
	v_pk_mul_f32 v[128:129], v[140:141], v[130:131] op_sel_hi:[0,1]
	v_pk_mul_f32 v[148:149], v[140:141], v[130:131] op_sel:[1,0]
	v_pk_fma_f32 v[94:95], v[140:141], v[120:121], v[94:95] op_sel_hi:[0,1,1]
	v_pk_fma_f32 v[128:129], v[142:143], v[120:121], v[128:129] op_sel_hi:[0,1,1]
	v_pk_fma_f32 v[148:149], v[142:143], v[120:121], v[148:149] op_sel:[1,0,0]
	v_pk_fma_f32 v[94:95], v[140:141], v[126:127], v[94:95] op_sel:[1,0,0]
	v_pk_fma_f32 v[128:129], v[142:143], v[126:127], v[128:129] op_sel:[1,0,0]
	v_pk_fma_f32 v[148:149], v[144:145], v[126:127], v[148:149] op_sel_hi:[0,1,1]
	v_pk_mul_f32 v[150:151], v[136:137], v[94:95] op_sel_hi:[0,1]
	v_pk_fma_f32 v[150:151], v[136:137], v[128:129], v[150:151] op_sel:[1,0,0]
	v_pk_fma_f32 v[150:151], v[138:139], v[148:149], v[150:151] op_sel_hi:[0,1,1]
	v_pk_fma_f32 v[150:151], v[144:145], v[60:61], v[150:151] op_sel:[1,0,0] neg_lo:[0,0,1] neg_hi:[0,0,1]
	v_cmp_eq_u32_e64 s[10:11], 6, v147
	v_cmp_eq_u32_e64 s[14:15], 7, v147
	v_pk_add_f32 v[60:61], v[58:59], v[94:95]
	v_pk_add_f32 v[120:121], v[80:81], v[60:61]
	v_pk_add_f32 v[58:59], v[82:83], v[128:129]
	v_pk_add_f32 v[80:81], v[92:93], v[58:59]
	v_pk_add_f32 v[82:83], v[122:123], v[148:149]
	v_pk_add_f32 v[92:93], v[152:153], v[82:83]
	v_pk_add_f32 v[122:123], v[124:125], v[150:151]
	v_pk_add_f32 v[126:127], v[154:155], v[122:123]
	v_pk_fma_f32 v[124:125], v[72:73], v[120:121], v[126:127] op_sel_hi:[0,1,1]
	v_pk_fma_f32 v[130:131], v[76:77], v[120:121], v[126:127] op_sel_hi:[0,1,1]
	v_pk_fma_f32 v[124:125], v[72:73], v[80:81], v[124:125] op_sel:[1,0,0]
	v_pk_fma_f32 v[130:131], v[76:77], v[80:81], v[130:131] op_sel:[1,0,0]
	v_pk_fma_f32 v[124:125], v[74:75], v[92:93], v[124:125] op_sel_hi:[0,1,1]
	v_pk_fma_f32 v[130:131], v[78:79], v[92:93], v[130:131] op_sel_hi:[0,1,1]
	v_pk_fma_f32 v[126:127], v[104:105], v[120:121], v[126:127] op_sel_hi:[0,1,1]
	v_pk_fma_f32 v[126:127], v[104:105], v[80:81], v[126:127] op_sel:[1,0,0]
	v_pk_fma_f32 v[126:127], v[106:107], v[92:93], v[126:127] op_sel_hi:[0,1,1]
	v_cndmask_b32_e64 v152, 0, v18, s[10:11]
	v_cndmask_b32_e64 v153, 0, v18, s[14:15]
	v_add_f32_dpp v126, v124, v126 wave_shl:1 row_mask:0xf bank_mask:0xf bound_ctrl:1
	v_add_f32_dpp v127, v125, v127 wave_shl:1 row_mask:0xf bank_mask:0xf bound_ctrl:1
	s_add_i32 s4, s34, 2
	s_cmpk_lt_i32 s4, 0x201
	s_cselect_b64 s[12:13], s[0:1], 0
	v_add_f32_dpp v126, v130, v126 wave_shr:1 row_mask:0xf bank_mask:0xf bound_ctrl:1
	v_add_f32_dpp v127, v131, v127 wave_shr:1 row_mask:0xf bank_mask:0xf bound_ctrl:1
	v_pk_fma_f32 v[126:127], v[48:49], v[146:147], v[126:127] op_sel_hi:[1,0,1] neg_lo:[0,0,1] neg_hi:[0,0,1]
	v_pk_add_f32 v[126:127], v[126:127], v[152:153] neg_lo:[0,1] neg_hi:[0,1]
	v_pk_mul_f32 v[154:155], v[126:127], v[126:127]
	v_add_f32_e32 v154, v154, v155
	v_cndmask_b32_e64 v155, 0, v154, s[12:13]
	v_add_f32_e32 v1, v1, v155
	s_add_i32 s5, s34, 7
	s_min_i32 s5, s5, 0x200
	s_mul_i32 s6, s5, 0x804
	s_add_i32 s6, s6, s35
	s_add_i32 s7, s6, 0x505014
	s_add_i32 s8, s6, 0x606018
	s_mul_i32 s9, s5, 0x180c
	s_add_i32 s9, s9, s33
	s_add_i32 s4, s34, 8
	s_min_i32 s4, s4, 0x200
	s_mul_i32 s4, s4, 0x804
	s_add_i32 s4, s4, s38
	buffer_load_dword v24, v28, s[20:23], s4 offen nt
	buffer_load_dwordx3 v[72:74], v27, s[24:27], s9 offen nt
	buffer_load_dword v48, v28, s[16:19], s7 offen nt
	buffer_load_dword v49, v28, s[16:19], s8 offen nt
	s_waitcnt vmcnt(8)
	v_mov_b32_dpp v76, v32 wave_shr:1 row_mask:0xf bank_mask:0xf bound_ctrl:1
	v_mov_b32_dpp v77, v33 wave_shr:1 row_mask:0xf bank_mask:0xf bound_ctrl:1
	v_mov_b32_dpp v78, v34 wave_shr:1 row_mask:0xf bank_mask:0xf bound_ctrl:1
	v_mov_b32_dpp v104, v32 wave_shl:1 row_mask:0xf bank_mask:0xf bound_ctrl:1
	v_mov_b32_dpp v105, v33 wave_shl:1 row_mask:0xf bank_mask:0xf bound_ctrl:1
	v_mov_b32_dpp v106, v34 wave_shl:1 row_mask:0xf bank_mask:0xf bound_ctrl:1
	s_add_i32 s4, s34, 6
	s_cmpk_lt_u32 s4, 0x201
	s_cselect_b64 s[12:13], s[40:41], 0
	v_cmp_eq_u32_e64 s[14:15], s37, v16
	s_and_b64 s[14:15], s[14:15], s[12:13]
	v_cndmask_b32_e64 v29, 0, 1, s[14:15]
	v_mul_f32_e64 v80, v32, v32
	v_mul_f32_e64 v81, v32, v33
	v_mul_f32_e64 v92, v32, v34
	v_mul_f32_e64 v93, v33, v33
	v_mul_f32_e64 v120, v33, v34
	v_mul_f32_e64 v121, v34, v34
	v_or_b32_dpp v31, v29, v29 wave_shr:1 row_mask:0xf bank_mask:0xf bound_ctrl:1
	s_nop 1
	v_or_b32_dpp v31, v29, v31 wave_shl:1 row_mask:0xf bank_mask:0xf bound_ctrl:1
	s_nop 1
	v_or_b32_dpp v84, v31, v31 wave_shr:1 row_mask:0xf bank_mask:0xf bound_ctrl:1
	s_nop 1
	v_or_b32_dpp v84, v31, v84 wave_shl:1 row_mask:0xf bank_mask:0xf bound_ctrl:1
	v_or3_b32 v29, v84, v85, v52
	v_or3_b32 v29, v29, v30, v53
	s_add_i32 s4, s34, 3
	s_cmpk_lt_u32 s4, 0x1ff
	s_cselect_b64 s[12:13], s[42:43], 0
	v_cmp_ne_u32_e64 s[30:31], 0, v29
	s_and_b64 s[30:31], s[30:31], s[12:13]
	v_cndmask_b32_e64 v29, 0, 1.0, s[30:31]
	v_add_f32_e64 v124, v32, v76
	v_add_f32_e64 v125, v33, v77
	v_add_f32_e64 v126, v34, v78
	v_fma_f32 v80, v76, v76, v80
	v_fma_f32 v81, v76, v77, v81
	v_fma_f32 v92, v76, v78, v92
	v_fma_f32 v93, v77, v77, v93
	v_fma_f32 v120, v77, v78, v120
	v_fma_f32 v121, v78, v78, v121
	v_add_f32_dpp v139, v29, v29 wave_shr:1 row_mask:0xf bank_mask:0xf bound_ctrl:1
	v_add_f32_e64 v124, v124, v104
	v_add_f32_e64 v125, v125, v105
	v_add_f32_e64 v126, v126, v106
	v_fma_f32 v127, v104, v104, v80
	v_fma_f32 v130, v104, v105, v81
	v_fma_f32 v131, v104, v106, v92
	v_fma_f32 v136, v105, v105, v93
	v_fma_f32 v137, v105, v106, v120
	v_fma_f32 v138, v106, v106, v121
	v_add_f32_dpp v139, v29, v139 wave_shl:1 row_mask:0xf bank_mask:0xf bound_ctrl:1
	v_pk_add_f32 v[80:81], v[38:39], v[124:125]
	v_pk_add_f32 v[38:39], v[54:55], v[126:127]
	v_pk_add_f32 v[54:55], v[108:109], v[130:131]
	v_pk_add_f32 v[92:93], v[112:113], v[136:137]
	v_pk_add_f32 v[108:109], v[114:115], v[138:139]
	v_mul_f32_e64 v112, v80, v22
	v_mul_f32_e64 v113, v81, v22
	v_mul_f32_e64 v114, v38, v22
	v_fma_f32 v29, v39, v22, v26
	v_mul_f32_e64 v31, v54, v22
	v_mul_f32_e64 v120, v55, v22
	v_fma_f32 v121, v92, v22, v26
	v_mul_f32_e64 v152, v93, v22
	v_fma_f32 v153, v108, v22, v26
	v_fma_f32 v29, -v112, v112, v29
	v_fma_f32 v31, -v112, v113, v31
	v_fma_f32 v120, -v112, v114, v120
	v_fma_f32 v121, -v113, v113, v121
	v_fma_f32 v152, -v113, v114, v152
	v_fma_f32 v153, -v114, v114, v153
	v_mul_f32_e64 v154, v152, v152
	v_mul_f32_e64 v155, v31, v153
	v_mul_f32_e64 v156, v120, v121
	v_mul_f32_e64 v157, v120, v120
	v_mul_f32_e64 v158, v29, v152
	v_mul_f32_e64 v159, v31, v31
	v_fma_f32 v154, v121, v153, -v154
	v_fma_f32 v155, v120, v152, -v155
	v_fma_f32 v156, v31, v152, -v156
	v_fma_f32 v157, v29, v153, -v157
	v_fma_f32 v158, v31, v120, -v158
	v_fma_f32 v159, v29, v121, -v159
	v_mul_f32_e64 v160, v29, v154
	v_fma_f32 v160, v31, v155, v160
	v_fma_f32 v160, v120, v156, v160
	v_rcp_f32_e32 v160, v160
	v_cmp_ne_u32_e64 vcc, s37, v17
	v_mul_f32_e64 v160, v160, v22
	v_cndmask_b32_e64 v160, 0, v160, s[30:31]
	v_cndmask_b32_e64 v29, 0, v18, vcc
	v_cndmask_b32_e64 v145, 0, v22, s[30:31]
	v_mul_f32_e64 v115, v154, v160
	v_mul_f32_e64 v140, v155, v160
	v_mul_f32_e64 v141, v156, v160
	v_mul_f32_e64 v142, v157, v160
	v_mul_f32_e64 v143, v158, v160
	v_mul_f32_e64 v144, v159, v160
	v_add_f32_e64 v146, v109, v29
	v_mov_b32_e32 v147, v17
	ds_write_b128 v23, v[112:115] offset:3072
	ds_write_b128 v23, v[140:143] offset:4096
	ds_write_b128 v23, v[144:147] offset:5120
	v_mov_b32_dpp v38, v20 wave_shr:1 row_mask:0xf bank_mask:0xf bound_ctrl:1
	v_mov_b32_dpp v39, v21 wave_shr:1 row_mask:0xf bank_mask:0xf bound_ctrl:1
	v_mov_b32_dpp v54, v20 wave_shl:1 row_mask:0xf bank_mask:0xf bound_ctrl:1
	v_mov_b32_dpp v55, v21 wave_shl:1 row_mask:0xf bank_mask:0xf bound_ctrl:1
	v_pk_mul_f32 v[80:81], v[20:21], v[32:33] op_sel_hi:[1,0]
	v_pk_mul_f32 v[92:93], v[20:21], v[32:33] op_sel:[0,1]
	v_pk_mul_f32 v[108:109], v[20:21], v[34:35] op_sel_hi:[1,0]
	v_pk_add_f32 v[120:121], v[20:21], v[38:39]
	v_pk_fma_f32 v[80:81], v[38:39], v[76:77], v[80:81] op_sel_hi:[1,0,1]
	v_pk_fma_f32 v[92:93], v[38:39], v[76:77], v[92:93] op_sel:[0,1,0]
	v_pk_fma_f32 v[108:109], v[38:39], v[78:79], v[108:109] op_sel_hi:[1,0,1]
	v_pk_add_f32 v[120:121], v[120:121], v[54:55]
	v_pk_fma_f32 v[80:81], v[54:55], v[104:105], v[80:81] op_sel_hi:[1,0,1]
	v_pk_fma_f32 v[92:93], v[54:55], v[104:105], v[92:93] op_sel:[0,1,0]
	v_pk_fma_f32 v[108:109], v[54:55], v[106:107], v[108:109] op_sel_hi:[1,0,1]
	s_waitcnt lgkmcnt(0)
	s_barrier
	v_pk_add_f32 v[38:39], v[50:51], v[120:121]
	v_pk_add_f32 v[50:51], v[118:119], v[80:81]
	v_pk_add_f32 v[54:55], v[64:65], v[92:93]
	v_pk_add_f32 v[64:65], v[90:91], v[108:109]
	v_pk_fma_f32 v[50:51], v[112:113], v[38:39], v[50:51] op_sel_hi:[0,1,1] neg_lo:[1,0,0] neg_hi:[1,0,0]
	v_pk_fma_f32 v[54:55], v[112:113], v[38:39], v[54:55] op_sel:[1,0,0] neg_lo:[1,0,0] neg_hi:[1,0,0]
	v_pk_fma_f32 v[64:65], v[114:115], v[38:39], v[64:65] op_sel_hi:[0,1,1] neg_lo:[1,0,0] neg_hi:[1,0,0]
	v_pk_mul_f32 v[90:91], v[114:115], v[50:51] op_sel:[1,0]
	v_pk_mul_f32 v[118:119], v[140:141], v[50:51] op_sel_hi:[0,1]
	v_pk_mul_f32 v[152:153], v[140:141], v[50:51] op_sel:[1,0]
	v_pk_fma_f32 v[90:91], v[140:141], v[54:55], v[90:91] op_sel_hi:[0,1,1]
	v_pk_fma_f32 v[118:119], v[142:143], v[54:55], v[118:119] op_sel_hi:[0,1,1]
	v_pk_fma_f32 v[152:153], v[142:143], v[54:55], v[152:153] op_sel:[1,0,0]
	v_pk_fma_f32 v[90:91], v[140:141], v[64:65], v[90:91] op_sel:[1,0,0]
	v_pk_fma_f32 v[118:119], v[142:143], v[64:65], v[118:119] op_sel:[1,0,0]
	v_pk_fma_f32 v[152:153], v[144:145], v[64:65], v[152:153] op_sel_hi:[0,1,1]
	v_pk_mul_f32 v[154:155], v[112:113], v[90:91] op_sel_hi:[0,1]
	v_pk_fma_f32 v[154:155], v[112:113], v[118:119], v[154:155] op_sel:[1,0,0]
	v_pk_fma_f32 v[154:155], v[114:115], v[152:153], v[154:155] op_sel_hi:[0,1,1]
	v_pk_fma_f32 v[154:155], v[144:145], v[38:39], v[154:155] op_sel:[1,0,0] neg_lo:[0,0,1] neg_hi:[0,0,1]
	v_cmp_eq_u32_e64 s[10:11], 6, v147
	v_cmp_eq_u32_e64 s[14:15], 7, v147
	v_pk_add_f32 v[38:39], v[60:61], v[90:91]
	v_pk_add_f32 v[50:51], v[58:59], v[118:119]
	v_pk_add_f32 v[54:55], v[82:83], v[152:153]
	v_pk_add_f32 v[58:59], v[122:123], v[154:155]
	v_pk_fma_f32 v[60:61], v[96:97], v[38:39], v[58:59] op_sel_hi:[0,1,1]
	v_pk_fma_f32 v[64:65], v[100:101], v[38:39], v[58:59] op_sel_hi:[0,1,1]
	v_pk_fma_f32 v[60:61], v[96:97], v[50:51], v[60:61] op_sel:[1,0,0]
	v_pk_fma_f32 v[64:65], v[100:101], v[50:51], v[64:65] op_sel:[1,0,0]
	v_pk_fma_f32 v[60:61], v[98:99], v[54:55], v[60:61] op_sel_hi:[0,1,1]
	v_pk_fma_f32 v[64:65], v[102:103], v[54:55], v[64:65] op_sel_hi:[0,1,1]
	v_pk_fma_f32 v[58:59], v[8:9], v[38:39], v[58:59] op_sel_hi:[0,1,1]
	v_pk_fma_f32 v[58:59], v[8:9], v[50:51], v[58:59] op_sel:[1,0,0]
	v_pk_fma_f32 v[58:59], v[10:11], v[54:55], v[58:59] op_sel_hi:[0,1,1]
	v_cndmask_b32_e64 v82, 0, v18, s[10:11]
	v_cndmask_b32_e64 v83, 0, v18, s[14:15]
	v_add_f32_dpp v58, v60, v58 wave_shl:1 row_mask:0xf bank_mask:0xf bound_ctrl:1
	v_add_f32_dpp v59, v61, v59 wave_shl:1 row_mask:0xf bank_mask:0xf bound_ctrl:1
	s_add_i32 s4, s34, 3
	s_cmpk_lt_i32 s4, 0x201
	s_cselect_b64 s[12:13], s[0:1], 0
	v_add_f32_dpp v58, v64, v58 wave_shr:1 row_mask:0xf bank_mask:0xf bound_ctrl:1
	v_add_f32_dpp v59, v65, v59 wave_shr:1 row_mask:0xf bank_mask:0xf bound_ctrl:1
	v_pk_fma_f32 v[58:59], v[4:5], v[146:147], v[58:59] op_sel_hi:[1,0,1] neg_lo:[0,0,1] neg_hi:[0,0,1]
	v_pk_add_f32 v[58:59], v[58:59], v[82:83] neg_lo:[0,1] neg_hi:[0,1]
	v_pk_mul_f32 v[122:123], v[58:59], v[58:59]
	v_add_f32_e32 v122, v122, v123
	v_cndmask_b32_e64 v123, 0, v122, s[12:13]
	v_add_f32_e32 v1, v1, v123
	s_add_i32 s5, s34, 8
	s_min_i32 s5, s5, 0x200
	s_mul_i32 s6, s5, 0x804
	s_add_i32 s6, s6, s35
	s_add_i32 s7, s6, 0x505014
	s_add_i32 s8, s6, 0x606018
	s_mul_i32 s9, s5, 0x180c
	s_add_i32 s9, s9, s33
	s_add_i32 s4, s34, 9
	s_min_i32 s4, s4, 0x200
	s_mul_i32 s4, s4, 0x804
	s_add_i32 s4, s4, s38
	buffer_load_dword v17, v28, s[20:23], s4 offen nt
	buffer_load_dwordx3 v[8:10], v27, s[24:27], s9 offen nt
	buffer_load_dword v4, v28, s[16:19], s7 offen nt
	buffer_load_dword v5, v28, s[16:19], s8 offen nt
	s_waitcnt vmcnt(8)
	v_mov_b32_dpp v96, v40 wave_shr:1 row_mask:0xf bank_mask:0xf bound_ctrl:1
	v_mov_b32_dpp v97, v41 wave_shr:1 row_mask:0xf bank_mask:0xf bound_ctrl:1
	v_mov_b32_dpp v98, v42 wave_shr:1 row_mask:0xf bank_mask:0xf bound_ctrl:1
	v_mov_b32_dpp v100, v40 wave_shl:1 row_mask:0xf bank_mask:0xf bound_ctrl:1
	v_mov_b32_dpp v101, v41 wave_shl:1 row_mask:0xf bank_mask:0xf bound_ctrl:1
	v_mov_b32_dpp v102, v42 wave_shl:1 row_mask:0xf bank_mask:0xf bound_ctrl:1
	s_add_i32 s4, s34, 7
	s_cmpk_lt_u32 s4, 0x201
	s_cselect_b64 s[12:13], s[40:41], 0
	v_cmp_eq_u32_e64 s[14:15], s37, v25
	s_and_b64 s[14:15], s[14:15], s[12:13]
	v_cndmask_b32_e64 v29, 0, 1, s[14:15]
	v_mul_f32_e64 v38, v40, v40
	v_mul_f32_e64 v39, v40, v41
	v_mul_f32_e64 v50, v40, v42
	v_mul_f32_e64 v51, v41, v41
	v_mul_f32_e64 v54, v41, v42
	v_mul_f32_e64 v55, v42, v42
	v_or_b32_dpp v31, v29, v29 wave_shr:1 row_mask:0xf bank_mask:0xf bound_ctrl:1
	s_nop 1
	v_or_b32_dpp v31, v29, v31 wave_shl:1 row_mask:0xf bank_mask:0xf bound_ctrl:1
	s_nop 1
	v_or_b32_dpp v53, v31, v31 wave_shr:1 row_mask:0xf bank_mask:0xf bound_ctrl:1
	s_nop 1
	v_or_b32_dpp v53, v31, v53 wave_shl:1 row_mask:0xf bank_mask:0xf bound_ctrl:1
	v_or3_b32 v29, v53, v84, v85
	v_or3_b32 v29, v29, v52, v30
	s_add_i32 s4, s34, 4
	s_cmpk_lt_u32 s4, 0x1ff
	s_cselect_b64 s[12:13], s[42:43], 0
	v_cmp_ne_u32_e64 s[30:31], 0, v29
	s_and_b64 s[30:31], s[30:31], s[12:13]
	v_cndmask_b32_e64 v29, 0, 1.0, s[30:31]
	v_add_f32_e64 v58, v40, v96
	v_add_f32_e64 v59, v41, v97
	v_add_f32_e64 v60, v42, v98
	v_fma_f32 v38, v96, v96, v38
	v_fma_f32 v39, v96, v97, v39
	v_fma_f32 v50, v96, v98, v50
	v_fma_f32 v51, v97, v97, v51
	v_fma_f32 v54, v97, v98, v54
	v_fma_f32 v55, v98, v98, v55
	v_add_f32_dpp v113, v29, v29 wave_shr:1 row_mask:0xf bank_mask:0xf bound_ctrl:1
	v_add_f32_e64 v58, v58, v100
	v_add_f32_e64 v59, v59, v101
	v_add_f32_e64 v60, v60, v102
	v_fma_f32 v61, v100, v100, v38
	v_fma_f32 v64, v100, v101, v39
	v_fma_f32 v65, v100, v102, v50
	v_fma_f32 v82, v101, v101, v51
	v_fma_f32 v83, v101, v102, v54
	v_fma_f32 v112, v102, v102, v55
	v_add_f32_dpp v113, v29, v113 wave_shl:1 row_mask:0xf bank_mask:0xf bound_ctrl:1
	v_pk_add_f32 v[38:39], v[124:125], v[58:59]
	v_pk_add_f32 v[50:51], v[56:57], v[38:39]
	v_pk_add_f32 v[54:55], v[126:127], v[60:61]
	v_pk_add_f32 v[56:57], v[62:63], v[54:55]
	v_pk_add_f32 v[62:63], v[130:131], v[64:65]
	v_pk_add_f32 v[114:115], v[66:67], v[62:63]
	v_pk_add_f32 v[66:67], v[136:137], v[82:83]
	v_pk_add_f32 v[122:123], v[86:87], v[66:67]
	v_pk_add_f32 v[86:87], v[138:139], v[112:113]
	v_pk_add_f32 v[124:125], v[88:89], v[86:87]
	v_mul_f32_e64 v136, v50, v22
	v_mul_f32_e64 v137, v51, v22
	v_mul_f32_e64 v138, v56, v22
	v_fma_f32 v29, v57, v22, v26
	v_mul_f32_e64 v31, v114, v22
	v_mul_f32_e64 v88, v115, v22
	v_fma_f32 v89, v122, v22, v26
	v_mul_f32_e64 v126, v123, v22
	v_fma_f32 v127, v124, v22, v26
	v_fma_f32 v29, -v136, v136, v29
	v_fma_f32 v31, -v136, v137, v31
	v_fma_f32 v88, -v136, v138, v88
	v_fma_f32 v89, -v137, v137, v89
	v_fma_f32 v126, -v137, v138, v126
	v_fma_f32 v127, -v138, v138, v127
	v_mul_f32_e64 v130, v126, v126
	v_mul_f32_e64 v131, v31, v127
	v_mul_f32_e64 v156, v88, v89
	v_mul_f32_e64 v157, v88, v88
	v_mul_f32_e64 v158, v29, v126
	v_mul_f32_e64 v159, v31, v31
	v_fma_f32 v130, v89, v127, -v130
	v_fma_f32 v131, v88, v126, -v131
	v_fma_f32 v156, v31, v126, -v156
	v_fma_f32 v157, v29, v127, -v157
	v_fma_f32 v158, v31, v88, -v158
	v_fma_f32 v159, v29, v89, -v159
	v_mul_f32_e64 v160, v29, v130
	v_fma_f32 v160, v31, v131, v160
	v_fma_f32 v160, v88, v156, v160
	v_rcp_f32_e32 v160, v160
	v_cmp_ne_u32_e64 vcc, s37, v2
	v_mul_f32_e64 v160, v160, v22
	v_cndmask_b32_e64 v160, 0, v160, s[30:31]
	v_cndmask_b32_e64 v29, 0, v18, vcc
	v_cndmask_b32_e64 v145, 0, v22, s[30:31]
	v_mul_f32_e64 v139, v130, v160
	v_mul_f32_e64 v140, v131, v160
	v_mul_f32_e64 v141, v156, v160
	v_mul_f32_e64 v142, v157, v160
	v_mul_f32_e64 v143, v158, v160
	v_mul_f32_e64 v144, v159, v160
	v_add_f32_e64 v146, v125, v29
	v_mov_b32_e32 v147, v2
	ds_write_b128 v23, v[136:139]
	ds_write_b128 v23, v[140:143] offset:1024
	ds_write_b128 v23, v[144:147] offset:2048
	v_mov_b32_dpp v30, v36 wave_shr:1 row_mask:0xf bank_mask:0xf bound_ctrl:1
	v_mov_b32_dpp v31, v37 wave_shr:1 row_mask:0xf bank_mask:0xf bound_ctrl:1
	v_mov_b32_dpp v50, v36 wave_shl:1 row_mask:0xf bank_mask:0xf bound_ctrl:1
	v_mov_b32_dpp v51, v37 wave_shl:1 row_mask:0xf bank_mask:0xf bound_ctrl:1
	v_pk_mul_f32 v[56:57], v[36:37], v[40:41] op_sel_hi:[1,0]
	v_pk_mul_f32 v[88:89], v[36:37], v[40:41] op_sel:[0,1]
	v_pk_mul_f32 v[114:115], v[36:37], v[42:43] op_sel_hi:[1,0]
	v_pk_add_f32 v[122:123], v[36:37], v[30:31]
	v_pk_fma_f32 v[56:57], v[30:31], v[96:97], v[56:57] op_sel_hi:[1,0,1]
	v_pk_fma_f32 v[88:89], v[30:31], v[96:97], v[88:89] op_sel:[0,1,0]
	v_pk_fma_f32 v[114:115], v[30:31], v[98:99], v[114:115] op_sel_hi:[1,0,1]
	v_pk_add_f32 v[122:123], v[122:123], v[50:51]
	v_pk_fma_f32 v[56:57], v[50:51], v[100:101], v[56:57] op_sel_hi:[1,0,1]
	v_pk_fma_f32 v[88:89], v[50:51], v[100:101], v[88:89] op_sel:[0,1,0]
	v_pk_fma_f32 v[114:115], v[50:51], v[102:103], v[114:115] op_sel_hi:[1,0,1]
	s_waitcnt lgkmcnt(0)
	s_barrier
	v_pk_add_f32 v[30:31], v[120:121], v[122:123]
	v_pk_add_f32 v[50:51], v[134:135], v[30:31]
	v_pk_add_f32 v[120:121], v[80:81], v[56:57]
	v_pk_add_f32 v[124:125], v[110:111], v[120:121]
	v_pk_add_f32 v[80:81], v[92:93], v[88:89]
	v_pk_add_f32 v[110:111], v[116:117], v[80:81]
	v_pk_add_f32 v[92:93], v[108:109], v[114:115]
	v_pk_add_f32 v[116:117], v[132:133], v[92:93]
	v_pk_fma_f32 v[124:125], v[136:137], v[50:51], v[124:125] op_sel_hi:[0,1,1] neg_lo:[1,0,0] neg_hi:[1,0,0]
	v_pk_fma_f32 v[110:111], v[136:137], v[50:51], v[110:111] op_sel:[1,0,0] neg_lo:[1,0,0] neg_hi:[1,0,0]
	v_pk_fma_f32 v[116:117], v[138:139], v[50:51], v[116:117] op_sel_hi:[0,1,1] neg_lo:[1,0,0] neg_hi:[1,0,0]
	v_pk_mul_f32 v[108:109], v[138:139], v[124:125] op_sel:[1,0]
	v_pk_mul_f32 v[126:127], v[140:141], v[124:125] op_sel_hi:[0,1]
	v_pk_mul_f32 v[130:131], v[140:141], v[124:125] op_sel:[1,0]
	v_pk_fma_f32 v[108:109], v[140:141], v[110:111], v[108:109] op_sel_hi:[0,1,1]
	v_pk_fma_f32 v[126:127], v[142:143], v[110:111], v[126:127] op_sel_hi:[0,1,1]
	v_pk_fma_f32 v[130:131], v[142:143], v[110:111], v[130:131] op_sel:[1,0,0]
	v_pk_fma_f32 v[108:109], v[140:141], v[116:117], v[108:109] op_sel:[1,0,0]
	v_pk_fma_f32 v[126:127], v[142:143], v[116:117], v[126:127] op_sel:[1,0,0]
	v_pk_fma_f32 v[130:131], v[144:145], v[116:117], v[130:131] op_sel_hi:[0,1,1]
	v_pk_mul_f32 v[132:133], v[136:137], v[108:109] op_sel_hi:[0,1]
	v_pk_fma_f32 v[132:133], v[136:137], v[126:127], v[132:133] op_sel:[1,0,0]
	v_pk_fma_f32 v[132:133], v[138:139], v[130:131], v[132:133] op_sel_hi:[0,1,1]
	v_pk_fma_f32 v[132:133], v[144:145], v[50:51], v[132:133] op_sel:[1,0,0] neg_lo:[0,0,1] neg_hi:[0,0,1]
	v_cmp_eq_u32_e64 s[10:11], 6, v147
	v_cmp_eq_u32_e64 s[14:15], 7, v147
	v_pk_add_f32 v[50:51], v[90:91], v[108:109]
	v_pk_add_f32 v[110:111], v[94:95], v[50:51]
	v_pk_add_f32 v[90:91], v[118:119], v[126:127]
	v_pk_add_f32 v[94:95], v[128:129], v[90:91]
	v_pk_add_f32 v[116:117], v[152:153], v[130:131]
	v_pk_add_f32 v[118:119], v[148:149], v[116:117]
	v_pk_add_f32 v[124:125], v[154:155], v[132:133]
	v_pk_add_f32 v[128:129], v[150:151], v[124:125]
	v_pk_fma_f32 v[134:135], v[44:45], v[110:111], v[128:129] op_sel_hi:[0,1,1]
	v_pk_fma_f32 v[148:149], v[68:69], v[110:111], v[128:129] op_sel_hi:[0,1,1]
	v_pk_fma_f32 v[134:135], v[44:45], v[94:95], v[134:135] op_sel:[1,0,0]
	v_pk_fma_f32 v[148:149], v[68:69], v[94:95], v[148:149] op_sel:[1,0,0]
	v_pk_fma_f32 v[134:135], v[46:47], v[118:119], v[134:135] op_sel_hi:[0,1,1]
	v_pk_fma_f32 v[148:149], v[70:71], v[118:119], v[148:149] op_sel_hi:[0,1,1]
	v_pk_fma_f32 v[128:129], v[12:13], v[110:111], v[128:129] op_sel_hi:[0,1,1]
	v_pk_fma_f32 v[128:129], v[12:13], v[94:95], v[128:129] op_sel:[1,0,0]
	v_pk_fma_f32 v[128:129], v[14:15], v[118:119], v[128:129] op_sel_hi:[0,1,1]
	v_cndmask_b32_e64 v150, 0, v18, s[10:11]
	v_cndmask_b32_e64 v151, 0, v18, s[14:15]
	v_add_f32_dpp v128, v134, v128 wave_shl:1 row_mask:0xf bank_mask:0xf bound_ctrl:1
	v_add_f32_dpp v129, v135, v129 wave_shl:1 row_mask:0xf bank_mask:0xf bound_ctrl:1
	s_add_i32 s4, s34, 4
	s_cmpk_lt_i32 s4, 0x201
	s_cselect_b64 s[12:13], s[0:1], 0
	v_add_f32_dpp v128, v148, v128 wave_shr:1 row_mask:0xf bank_mask:0xf bound_ctrl:1
	v_add_f32_dpp v129, v149, v129 wave_shr:1 row_mask:0xf bank_mask:0xf bound_ctrl:1
	v_pk_fma_f32 v[128:129], v[6:7], v[146:147], v[128:129] op_sel_hi:[1,0,1] neg_lo:[0,0,1] neg_hi:[0,0,1]
	v_pk_add_f32 v[128:129], v[128:129], v[150:151] neg_lo:[0,1] neg_hi:[0,1]
	v_pk_mul_f32 v[152:153], v[128:129], v[128:129]
	v_add_f32_e32 v152, v152, v153
	v_cndmask_b32_e64 v153, 0, v152, s[12:13]
	v_add_f32_e32 v1, v1, v153
	s_add_i32 s5, s34, 9
	s_min_i32 s5, s5, 0x200
	s_mul_i32 s6, s5, 0x804
	s_add_i32 s6, s6, s35
	s_add_i32 s7, s6, 0x505014
	s_add_i32 s8, s6, 0x606018
	s_mul_i32 s9, s5, 0x180c
	s_add_i32 s9, s9, s33
	s_add_i32 s4, s34, 10
	s_min_i32 s4, s4, 0x200
	s_mul_i32 s4, s4, 0x804
	s_add_i32 s4, s4, s38
	buffer_load_dword v2, v28, s[20:23], s4 offen nt
	buffer_load_dwordx3 v[12:14], v27, s[24:27], s9 offen nt
	buffer_load_dword v6, v28, s[16:19], s7 offen nt
	buffer_load_dword v7, v28, s[16:19], s8 offen nt
	s_waitcnt vmcnt(8)
	v_mov_b32_dpp v44, v72 wave_shr:1 row_mask:0xf bank_mask:0xf bound_ctrl:1
	v_mov_b32_dpp v45, v73 wave_shr:1 row_mask:0xf bank_mask:0xf bound_ctrl:1
	v_mov_b32_dpp v46, v74 wave_shr:1 row_mask:0xf bank_mask:0xf bound_ctrl:1
	v_mov_b32_dpp v68, v72 wave_shl:1 row_mask:0xf bank_mask:0xf bound_ctrl:1
	v_mov_b32_dpp v69, v73 wave_shl:1 row_mask:0xf bank_mask:0xf bound_ctrl:1
	v_mov_b32_dpp v70, v74 wave_shl:1 row_mask:0xf bank_mask:0xf bound_ctrl:1
	s_add_i32 s4, s34, 8
	s_cmpk_lt_u32 s4, 0x201
	s_cselect_b64 s[12:13], s[40:41], 0
	v_cmp_eq_u32_e64 s[14:15], s37, v24
	s_and_b64 s[14:15], s[14:15], s[12:13]
	v_cndmask_b32_e64 v29, 0, 1, s[14:15]
	v_mul_f32_e64 v94, v72, v72
	v_mul_f32_e64 v95, v72, v73
	v_mul_f32_e64 v110, v72, v74
	v_mul_f32_e64 v111, v73, v73
	v_mul_f32_e64 v118, v73, v74
	v_mul_f32_e64 v119, v74, v74
	v_or_b32_dpp v128, v29, v29 wave_shr:1 row_mask:0xf bank_mask:0xf bound_ctrl:1
	s_nop 1
	v_or_b32_dpp v128, v29, v128 wave_shl:1 row_mask:0xf bank_mask:0xf bound_ctrl:1
	s_nop 1
	v_or_b32_dpp v129, v128, v128 wave_shr:1 row_mask:0xf bank_mask:0xf bound_ctrl:1
	s_nop 1
	v_or_b32_dpp v129, v128, v129 wave_shl:1 row_mask:0xf bank_mask:0xf bound_ctrl:1
	v_or3_b32 v29, v129, v53, v84
	v_or3_b32 v29, v29, v85, v52
	s_add_i32 s4, s34, 5
	s_cmpk_lt_u32 s4, 0x1ff
	s_cselect_b64 s[12:13], s[42:43], 0
	v_cmp_ne_u32_e64 s[30:31], 0, v29
	s_and_b64 s[30:31], s[30:31], s[12:13]
	v_cndmask_b32_e64 v29, 0, 1.0, s[30:31]
	v_add_f32_e64 v134, v72, v44
	v_add_f32_e64 v135, v73, v45
	v_add_f32_e64 v136, v74, v46
	v_fma_f32 v94, v44, v44, v94
	v_fma_f32 v95, v44, v45, v95
	v_fma_f32 v110, v44, v46, v110
	v_fma_f32 v111, v45, v45, v111
	v_fma_f32 v118, v45, v46, v118
	v_fma_f32 v119, v46, v46, v119
	v_add_f32_dpp v143, v29, v29 wave_shr:1 row_mask:0xf bank_mask:0xf bound_ctrl:1
	v_add_f32_e64 v134, v134, v68
	v_add_f32_e64 v135, v135, v69
	v_add_f32_e64 v136, v136, v70
	v_fma_f32 v137, v68, v68, v94
	v_fma_f32 v138, v68, v69, v95
	v_fma_f32 v139, v68, v70, v110
	v_fma_f32 v140, v69, v69, v111
	v_fma_f32 v141, v69, v70, v118
	v_fma_f32 v142, v70, v70, v119
	v_add_f32_dpp v143, v29, v143 wave_shl:1 row_mask:0xf bank_mask:0xf bound_ctrl:1
	v_pk_add_f32 v[94:95], v[38:39], v[134:135]
	v_pk_add_f32 v[38:39], v[54:55], v[136:137]
	v_pk_add_f32 v[54:55], v[62:63], v[138:139]
	v_pk_add_f32 v[62:63], v[66:67], v[140:141]
	v_pk_add_f32 v[66:67], v[86:87], v[142:143]
	v_mul_f32_e64 v144, v94, v22
	v_mul_f32_e64 v145, v95, v22
	v_mul_f32_e64 v146, v38, v22
	v_fma_f32 v29, v39, v22, v26
	v_mul_f32_e64 v128, v54, v22
	v_mul_f32_e64 v86, v55, v22
	v_fma_f32 v87, v62, v22, v26
	v_mul_f32_e64 v110, v63, v22
	v_fma_f32 v111, v66, v22, v26
	v_fma_f32 v29, -v144, v144, v29
	v_fma_f32 v128, -v144, v145, v128
	v_fma_f32 v86, -v144, v146, v86
	v_fma_f32 v87, -v145, v145, v87
	v_fma_f32 v110, -v145, v146, v110
	v_fma_f32 v111, -v146, v146, v111
	v_mul_f32_e64 v118, v110, v110
	v_mul_f32_e64 v119, v128, v111
	v_mul_f32_e64 v156, v86, v87
	v_mul_f32_e64 v157, v86, v86
	v_mul_f32_e64 v158, v29, v110
	v_mul_f32_e64 v159, v128, v128
	v_fma_f32 v118, v87, v111, -v118
	v_fma_f32 v119, v86, v110, -v119
	v_fma_f32 v156, v128, v110, -v156
	v_fma_f32 v157, v29, v111, -v157
	v_fma_f32 v158, v128, v86, -v158
	v_fma_f32 v159, v29, v87, -v159
	v_mul_f32_e64 v160, v29, v118
	v_fma_f32 v160, v128, v119, v160
	v_fma_f32 v160, v86, v156, v160
	v_rcp_f32_e32 v160, v160
	v_cmp_ne_u32_e64 vcc, s37, v3
	v_mul_f32_e64 v160, v160, v22
	v_cndmask_b32_e64 v160, 0, v160, s[30:31]
	v_cndmask_b32_e64 v29, 0, v18, vcc
	v_cndmask_b32_e64 v153, 0, v22, s[30:31]
	v_mul_f32_e64 v147, v118, v160
	v_mul_f32_e64 v148, v119, v160
	v_mul_f32_e64 v149, v156, v160
	v_mul_f32_e64 v150, v157, v160
	v_mul_f32_e64 v151, v158, v160
	v_mul_f32_e64 v152, v159, v160
	v_add_f32_e64 v154, v67, v29
	v_mov_b32_e32 v155, v3
	ds_write_b128 v23, v[144:147] offset:3072
	ds_write_b128 v23, v[148:151] offset:4096
	ds_write_b128 v23, v[152:155] offset:5120
	v_mov_b32_dpp v38, v48 wave_shr:1 row_mask:0xf bank_mask:0xf bound_ctrl:1
	v_mov_b32_dpp v39, v49 wave_shr:1 row_mask:0xf bank_mask:0xf bound_ctrl:1
	v_mov_b32_dpp v54, v48 wave_shl:1 row_mask:0xf bank_mask:0xf bound_ctrl:1
	v_mov_b32_dpp v55, v49 wave_shl:1 row_mask:0xf bank_mask:0xf bound_ctrl:1
	v_pk_mul_f32 v[62:63], v[48:49], v[72:73] op_sel_hi:[1,0]
	v_pk_mul_f32 v[66:67], v[48:49], v[72:73] op_sel:[0,1]
	v_pk_mul_f32 v[86:87], v[48:49], v[74:75] op_sel_hi:[1,0]
	v_pk_add_f32 v[94:95], v[48:49], v[38:39]
	v_pk_fma_f32 v[62:63], v[38:39], v[44:45], v[62:63] op_sel_hi:[1,0,1]
	v_pk_fma_f32 v[66:67], v[38:39], v[44:45], v[66:67] op_sel:[0,1,0]
	v_pk_fma_f32 v[86:87], v[38:39], v[46:47], v[86:87] op_sel_hi:[1,0,1]
	v_pk_add_f32 v[94:95], v[94:95], v[54:55]
	v_pk_fma_f32 v[62:63], v[54:55], v[68:69], v[62:63] op_sel_hi:[1,0,1]
	v_pk_fma_f32 v[66:67], v[54:55], v[68:69], v[66:67] op_sel:[0,1,0]
	v_pk_fma_f32 v[86:87], v[54:55], v[70:71], v[86:87] op_sel_hi:[1,0,1]
	s_waitcnt lgkmcnt(0)
	s_barrier
	v_pk_add_f32 v[38:39], v[30:31], v[94:95]
	v_pk_add_f32 v[30:31], v[120:121], v[62:63]
	v_pk_add_f32 v[54:55], v[80:81], v[66:67]
	v_pk_add_f32 v[80:81], v[92:93], v[86:87]
	v_pk_fma_f32 v[30:31], v[144:145], v[38:39], v[30:31] op_sel_hi:[0,1,1] neg_lo:[1,0,0] neg_hi:[1,0,0]
	v_pk_fma_f32 v[54:55], v[144:145], v[38:39], v[54:55] op_sel:[1,0,0] neg_lo:[1,0,0] neg_hi:[1,0,0]
	v_pk_fma_f32 v[80:81], v[146:147], v[38:39], v[80:81] op_sel_hi:[0,1,1] neg_lo:[1,0,0] neg_hi:[1,0,0]
	v_pk_mul_f32 v[92:93], v[146:147], v[30:31] op_sel:[1,0]
	v_pk_mul_f32 v[110:111], v[148:149], v[30:31] op_sel_hi:[0,1]
	v_pk_mul_f32 v[118:119], v[148:149], v[30:31] op_sel:[1,0]
	v_pk_fma_f32 v[92:93], v[148:149], v[54:55], v[92:93] op_sel_hi:[0,1,1]
	v_pk_fma_f32 v[110:111], v[150:151], v[54:55], v[110:111] op_sel_hi:[0,1,1]
	v_pk_fma_f32 v[118:119], v[150:151], v[54:55], v[118:119] op_sel:[1,0,0]
	v_pk_fma_f32 v[92:93], v[148:149], v[80:81], v[92:93] op_sel:[1,0,0]
	v_pk_fma_f32 v[110:111], v[150:151], v[80:81], v[110:111] op_sel:[1,0,0]
	v_pk_fma_f32 v[118:119], v[152:153], v[80:81], v[118:119] op_sel_hi:[0,1,1]
	v_pk_mul_f32 v[120:121], v[144:145], v[92:93] op_sel_hi:[0,1]
	v_pk_fma_f32 v[120:121], v[144:145], v[110:111], v[120:121] op_sel:[1,0,0]
	v_pk_fma_f32 v[120:121], v[146:147], v[118:119], v[120:121] op_sel_hi:[0,1,1]
	v_pk_fma_f32 v[120:121], v[152:153], v[38:39], v[120:121] op_sel:[1,0,0] neg_lo:[0,0,1] neg_hi:[0,0,1]
	v_cmp_eq_u32_e64 s[10:11], 6, v155
	v_cmp_eq_u32_e64 s[14:15], 7, v155
	v_pk_add_f32 v[30:31], v[50:51], v[92:93]
	v_pk_add_f32 v[38:39], v[90:91], v[110:111]
	v_pk_add_f32 v[50:51], v[116:117], v[118:119]
	v_pk_add_f32 v[54:55], v[124:125], v[120:121]
	v_pk_fma_f32 v[80:81], v[76:77], v[30:31], v[54:55] op_sel_hi:[0,1,1]
	v_pk_fma_f32 v[90:91], v[104:105], v[30:31], v[54:55] op_sel_hi:[0,1,1]
	v_pk_fma_f32 v[80:81], v[76:77], v[38:39], v[80:81] op_sel:[1,0,0]
	v_pk_fma_f32 v[90:91], v[104:105], v[38:39], v[90:91] op_sel:[1,0,0]
	v_pk_fma_f32 v[80:81], v[78:79], v[50:51], v[80:81] op_sel_hi:[0,1,1]
	v_pk_fma_f32 v[90:91], v[106:107], v[50:51], v[90:91] op_sel_hi:[0,1,1]
	v_pk_fma_f32 v[54:55], v[32:33], v[30:31], v[54:55] op_sel_hi:[0,1,1]
	v_pk_fma_f32 v[54:55], v[32:33], v[38:39], v[54:55] op_sel:[1,0,0]
	v_pk_fma_f32 v[54:55], v[34:35], v[50:51], v[54:55] op_sel_hi:[0,1,1]
	v_cndmask_b32_e64 v116, 0, v18, s[10:11]
	v_cndmask_b32_e64 v117, 0, v18, s[14:15]
	v_add_f32_dpp v54, v80, v54 wave_shl:1 row_mask:0xf bank_mask:0xf bound_ctrl:1
	v_add_f32_dpp v55, v81, v55 wave_shl:1 row_mask:0xf bank_mask:0xf bound_ctrl:1
	s_add_i32 s4, s34, 5
	s_cmpk_lt_i32 s4, 0x201
	s_cselect_b64 s[12:13], s[0:1], 0
	v_add_f32_dpp v54, v90, v54 wave_shr:1 row_mask:0xf bank_mask:0xf bound_ctrl:1
	v_add_f32_dpp v55, v91, v55 wave_shr:1 row_mask:0xf bank_mask:0xf bound_ctrl:1
	v_pk_fma_f32 v[54:55], v[20:21], v[154:155], v[54:55] op_sel_hi:[1,0,1] neg_lo:[0,0,1] neg_hi:[0,0,1]
	v_pk_add_f32 v[54:55], v[54:55], v[116:117] neg_lo:[0,1] neg_hi:[0,1]
	v_pk_mul_f32 v[124:125], v[54:55], v[54:55]
	v_add_f32_e32 v124, v124, v125
	v_cndmask_b32_e64 v125, 0, v124, s[12:13]
	v_add_f32_e32 v1, v1, v125
	s_add_i32 s5, s34, 10
	s_min_i32 s5, s5, 0x200
	s_mul_i32 s6, s5, 0x804
	s_add_i32 s6, s6, s35
	s_add_i32 s7, s6, 0x505014
	s_add_i32 s8, s6, 0x606018
	s_mul_i32 s9, s5, 0x180c
	s_add_i32 s9, s9, s33
	s_add_i32 s4, s34, 11
	s_min_i32 s4, s4, 0x200
	s_mul_i32 s4, s4, 0x804
	s_add_i32 s4, s4, s38
	buffer_load_dword v3, v28, s[20:23], s4 offen nt
	buffer_load_dwordx3 v[32:34], v27, s[24:27], s9 offen nt
	buffer_load_dword v20, v28, s[16:19], s7 offen nt
	buffer_load_dword v21, v28, s[16:19], s8 offen nt
	s_waitcnt vmcnt(8)
	v_mov_b32_dpp v76, v8 wave_shr:1 row_mask:0xf bank_mask:0xf bound_ctrl:1
	v_mov_b32_dpp v77, v9 wave_shr:1 row_mask:0xf bank_mask:0xf bound_ctrl:1
	v_mov_b32_dpp v78, v10 wave_shr:1 row_mask:0xf bank_mask:0xf bound_ctrl:1
	v_mov_b32_dpp v104, v8 wave_shl:1 row_mask:0xf bank_mask:0xf bound_ctrl:1
	v_mov_b32_dpp v105, v9 wave_shl:1 row_mask:0xf bank_mask:0xf bound_ctrl:1
	v_mov_b32_dpp v106, v10 wave_shl:1 row_mask:0xf bank_mask:0xf bound_ctrl:1
	s_add_i32 s4, s34, 9
	s_cmpk_lt_u32 s4, 0x201
	s_cselect_b64 s[12:13], s[40:41], 0
	v_cmp_eq_u32_e64 s[14:15], s37, v17
	s_and_b64 s[14:15], s[14:15], s[12:13]
	v_cndmask_b32_e64 v29, 0, 1, s[14:15]
	v_mul_f32_e64 v30, v8, v8
	v_mul_f32_e64 v31, v8, v9
	v_mul_f32_e64 v38, v8, v10
	v_mul_f32_e64 v39, v9, v9
	v_mul_f32_e64 v50, v9, v10
	v_mul_f32_e64 v51, v10, v10
	v_or_b32_dpp v52, v29, v29 wave_shr:1 row_mask:0xf bank_mask:0xf bound_ctrl:1
	s_nop 1
	v_or_b32_dpp v52, v29, v52 wave_shl:1 row_mask:0xf bank_mask:0xf bound_ctrl:1
	s_nop 1
	v_or_b32_dpp v128, v52, v52 wave_shr:1 row_mask:0xf bank_mask:0xf bound_ctrl:1
	s_nop 1
	v_or_b32_dpp v128, v52, v128 wave_shl:1 row_mask:0xf bank_mask:0xf bound_ctrl:1
	v_or3_b32 v29, v128, v129, v53
	v_or3_b32 v29, v29, v84, v85
	s_add_i32 s4, s34, 6
	s_cmpk_lt_u32 s4, 0x1ff
	s_cselect_b64 s[12:13], s[42:43], 0
	v_cmp_ne_u32_e64 s[30:31], 0, v29
	s_and_b64 s[30:31], s[30:31], s[12:13]
	v_cndmask_b32_e64 v29, 0, 1.0, s[30:31]
	v_add_f32_e64 v54, v8, v76
	v_add_f32_e64 v55, v9, v77
	v_add_f32_e64 v80, v10, v78
	v_fma_f32 v30, v76, v76, v30
	v_fma_f32 v31, v76, v77, v31
	v_fma_f32 v38, v76, v78, v38
	v_fma_f32 v39, v77, v77, v39
	v_fma_f32 v50, v77, v78, v50
	v_fma_f32 v51, v78, v78, v51
	v_add_f32_dpp v125, v29, v29 wave_shr:1 row_mask:0xf bank_mask:0xf bound_ctrl:1
	v_add_f32_e64 v54, v54, v104
	v_add_f32_e64 v55, v55, v105
	v_add_f32_e64 v80, v80, v106
	v_fma_f32 v81, v104, v104, v30
	v_fma_f32 v90, v104, v105, v31
	v_fma_f32 v91, v104, v106, v38
	v_fma_f32 v116, v105, v105, v39
	v_fma_f32 v117, v105, v106, v50
	v_fma_f32 v124, v106, v106, v51
	v_add_f32_dpp v125, v29, v125 wave_shl:1 row_mask:0xf bank_mask:0xf bound_ctrl:1
	v_pk_add_f32 v[30:31], v[134:135], v[54:55]
	v_pk_add_f32 v[38:39], v[58:59], v[30:31]
	v_pk_add_f32 v[50:51], v[136:137], v[80:81]
	v_pk_add_f32 v[58:59], v[60:61], v[50:51]
	v_pk_add_f32 v[60:61], v[138:139], v[90:91]
	v_pk_add_f32 v[134:135], v[64:65], v[60:61]
	v_pk_add_f32 v[64:65], v[140:141], v[116:117]
	v_pk_add_f32 v[136:137], v[82:83], v[64:65]
	v_pk_add_f32 v[82:83], v[142:143], v[124:125]
	v_pk_add_f32 v[138:139], v[112:113], v[82:83]
	v_mul_f32_e64 v140, v38, v22
	v_mul_f32_e64 v141, v39, v22
	v_mul_f32_e64 v142, v58, v22
	v_fma_f32 v29, v59, v22, v26
	v_mul_f32_e64 v52, v134, v22
	v_mul_f32_e64 v112, v135, v22
	v_fma_f32 v113, v136, v22, v26
	v_mul_f32_e64 v152, v137, v22
	v_fma_f32 v153, v138, v22, v26
	v_fma_f32 v29, -v140, v140, v29
	v_fma_f32 v52, -v140, v141, v52
	v_fma_f32 v112, -v140, v142, v112
	v_fma_f32 v113, -v141, v141, v113
	v_fma_f32 v152, -v141, v142, v152
	v_fma_f32 v153, -v142, v142, v153
	v_mul_f32_e64 v154, v152, v152
	v_mul_f32_e64 v155, v52, v153
	v_mul_f32_e64 v156, v112, v113
	v_mul_f32_e64 v157, v112, v112
	v_mul_f32_e64 v158, v29, v152
	v_mul_f32_e64 v159, v52, v52
	v_fma_f32 v154, v113, v153, -v154
	v_fma_f32 v155, v112, v152, -v155
	v_fma_f32 v156, v52, v152, -v156
	v_fma_f32 v157, v29, v153, -v157
	v_fma_f32 v158, v52, v112, -v158
	v_fma_f32 v159, v29, v113, -v159
	v_mul_f32_e64 v160, v29, v154
	v_fma_f32 v160, v52, v155, v160
	v_fma_f32 v160, v112, v156, v160
	v_rcp_f32_e32 v160, v160
	v_cmp_ne_u32_e64 vcc, s37, v16
	v_mul_f32_e64 v160, v160, v22
	v_cndmask_b32_e64 v160, 0, v160, s[30:31]
	v_cndmask_b32_e64 v29, 0, v18, vcc
	v_cndmask_b32_e64 v149, 0, v22, s[30:31]
	v_mul_f32_e64 v143, v154, v160
	v_mul_f32_e64 v144, v155, v160
	v_mul_f32_e64 v145, v156, v160
	v_mul_f32_e64 v146, v157, v160
	v_mul_f32_e64 v147, v158, v160
	v_mul_f32_e64 v148, v159, v160
	v_add_f32_e64 v150, v139, v29
	v_mov_b32_e32 v151, v16
	ds_write_b128 v23, v[140:143]
	ds_write_b128 v23, v[144:147] offset:1024
	ds_write_b128 v23, v[148:151] offset:2048
	v_mov_b32_dpp v38, v4 wave_shr:1 row_mask:0xf bank_mask:0xf bound_ctrl:1
	v_mov_b32_dpp v39, v5 wave_shr:1 row_mask:0xf bank_mask:0xf bound_ctrl:1
	v_mov_b32_dpp v58, v4 wave_shl:1 row_mask:0xf bank_mask:0xf bound_ctrl:1
	v_mov_b32_dpp v59, v5 wave_shl:1 row_mask:0xf bank_mask:0xf bound_ctrl:1
	v_pk_mul_f32 v[112:113], v[4:5], v[8:9] op_sel_hi:[1,0]
	v_pk_mul_f32 v[134:135], v[4:5], v[8:9] op_sel:[0,1]
	v_pk_mul_f32 v[136:137], v[4:5], v[10:11] op_sel_hi:[1,0]
	v_pk_add_f32 v[138:139], v[4:5], v[38:39]
	v_pk_fma_f32 v[112:113], v[38:39], v[76:77], v[112:113] op_sel_hi:[1,0,1]
	v_pk_fma_f32 v[134:135], v[38:39], v[76:77], v[134:135] op_sel:[0,1,0]
	v_pk_fma_f32 v[136:137], v[38:39], v[78:79], v[136:137] op_sel_hi:[1,0,1]
	v_pk_add_f32 v[138:139], v[138:139], v[58:59]
	v_pk_fma_f32 v[112:113], v[58:59], v[104:105], v[112:113] op_sel_hi:[1,0,1]
	v_pk_fma_f32 v[134:135], v[58:59], v[104:105], v[134:135] op_sel:[0,1,0]
	v_pk_fma_f32 v[136:137], v[58:59], v[106:107], v[136:137] op_sel_hi:[1,0,1]
	s_waitcnt lgkmcnt(0)
	s_barrier
	v_pk_add_f32 v[38:39], v[94:95], v[138:139]
	v_pk_add_f32 v[58:59], v[122:123], v[38:39]
	v_pk_add_f32 v[94:95], v[62:63], v[112:113]
	v_pk_add_f32 v[122:123], v[56:57], v[94:95]
	v_pk_add_f32 v[56:57], v[66:67], v[134:135]
	v_pk_add_f32 v[62:63], v[88:89], v[56:57]
	v_pk_add_f32 v[66:67], v[86:87], v[136:137]
	v_pk_add_f32 v[88:89], v[114:115], v[66:67]
	v_pk_fma_f32 v[122:123], v[140:141], v[58:59], v[122:123] op_sel_hi:[0,1,1] neg_lo:[1,0,0] neg_hi:[1,0,0]
	v_pk_fma_f32 v[62:63], v[140:141], v[58:59], v[62:63] op_sel:[1,0,0] neg_lo:[1,0,0] neg_hi:[1,0,0]
	v_pk_fma_f32 v[88:89], v[142:143], v[58:59], v[88:89] op_sel_hi:[0,1,1] neg_lo:[1,0,0] neg_hi:[1,0,0]
	v_pk_mul_f32 v[86:87], v[142:143], v[122:123] op_sel:[1,0]
	v_pk_mul_f32 v[114:115], v[144:145], v[122:123] op_sel_hi:[0,1]
	v_pk_mul_f32 v[152:153], v[144:145], v[122:123] op_sel:[1,0]
	v_pk_fma_f32 v[86:87], v[144:145], v[62:63], v[86:87] op_sel_hi:[0,1,1]
	v_pk_fma_f32 v[114:115], v[146:147], v[62:63], v[114:115] op_sel_hi:[0,1,1]
	v_pk_fma_f32 v[152:153], v[146:147], v[62:63], v[152:153] op_sel:[1,0,0]
	v_pk_fma_f32 v[86:87], v[144:145], v[88:89], v[86:87] op_sel:[1,0,0]
	v_pk_fma_f32 v[114:115], v[146:147], v[88:89], v[114:115] op_sel:[1,0,0]
	v_pk_fma_f32 v[152:153], v[148:149], v[88:89], v[152:153] op_sel_hi:[0,1,1]
	v_pk_mul_f32 v[154:155], v[140:141], v[86:87] op_sel_hi:[0,1]
	v_pk_fma_f32 v[154:155], v[140:141], v[114:115], v[154:155] op_sel:[1,0,0]
	v_pk_fma_f32 v[154:155], v[142:143], v[152:153], v[154:155] op_sel_hi:[0,1,1]
	v_pk_fma_f32 v[154:155], v[148:149], v[58:59], v[154:155] op_sel:[1,0,0] neg_lo:[0,0,1] neg_hi:[0,0,1]
	v_cmp_eq_u32_e64 s[10:11], 6, v151
	v_cmp_eq_u32_e64 s[14:15], 7, v151
	v_pk_add_f32 v[58:59], v[92:93], v[86:87]
	v_pk_add_f32 v[62:63], v[108:109], v[58:59]
	v_pk_add_f32 v[88:89], v[110:111], v[114:115]
	v_pk_add_f32 v[92:93], v[126:127], v[88:89]
	v_pk_add_f32 v[108:109], v[118:119], v[152:153]
	v_pk_add_f32 v[110:111], v[130:131], v[108:109]
	v_pk_add_f32 v[118:119], v[120:121], v[154:155]
	v_pk_add_f32 v[122:123], v[132:133], v[118:119]
	v_pk_fma_f32 v[120:121], v[96:97], v[62:63], v[122:123] op_sel_hi:[0,1,1]
	v_pk_fma_f32 v[126:127], v[100:101], v[62:63], v[122:123] op_sel_hi:[0,1,1]
	v_pk_fma_f32 v[120:121], v[96:97], v[92:93], v[120:121] op_sel:[1,0,0]
	v_pk_fma_f32 v[126:127], v[100:101], v[92:93], v[126:127] op_sel:[1,0,0]
	v_pk_fma_f32 v[120:121], v[98:99], v[110:111], v[120:121] op_sel_hi:[0,1,1]
	v_pk_fma_f32 v[126:127], v[102:103], v[110:111], v[126:127] op_sel_hi:[0,1,1]
	v_pk_fma_f32 v[122:123], v[40:41], v[62:63], v[122:123] op_sel_hi:[0,1,1]
	v_pk_fma_f32 v[122:123], v[40:41], v[92:93], v[122:123] op_sel:[1,0,0]
	v_pk_fma_f32 v[122:123], v[42:43], v[110:111], v[122:123] op_sel_hi:[0,1,1]
	v_cndmask_b32_e64 v130, 0, v18, s[10:11]
	v_cndmask_b32_e64 v131, 0, v18, s[14:15]
	v_add_f32_dpp v122, v120, v122 wave_shl:1 row_mask:0xf bank_mask:0xf bound_ctrl:1
	v_add_f32_dpp v123, v121, v123 wave_shl:1 row_mask:0xf bank_mask:0xf bound_ctrl:1
	s_add_i32 s4, s34, 6
	s_cmpk_lt_i32 s4, 0x201
	s_cselect_b64 s[12:13], s[0:1], 0
	v_add_f32_dpp v122, v126, v122 wave_shr:1 row_mask:0xf bank_mask:0xf bound_ctrl:1
	v_add_f32_dpp v123, v127, v123 wave_shr:1 row_mask:0xf bank_mask:0xf bound_ctrl:1
	v_pk_fma_f32 v[122:123], v[36:37], v[150:151], v[122:123] op_sel_hi:[1,0,1] neg_lo:[0,0,1] neg_hi:[0,0,1]
	v_pk_add_f32 v[122:123], v[122:123], v[130:131] neg_lo:[0,1] neg_hi:[0,1]
	v_pk_mul_f32 v[132:133], v[122:123], v[122:123]
	v_add_f32_e32 v132, v132, v133
	v_cndmask_b32_e64 v133, 0, v132, s[12:13]
	v_add_f32_e32 v1, v1, v133
	s_add_i32 s5, s34, 11
	s_min_i32 s5, s5, 0x200
	s_mul_i32 s6, s5, 0x804
	s_add_i32 s6, s6, s35
	s_add_i32 s7, s6, 0x505014
	s_add_i32 s8, s6, 0x606018
	s_mul_i32 s9, s5, 0x180c
	s_add_i32 s9, s9, s33
	s_add_i32 s4, s34, 12
	s_min_i32 s4, s4, 0x200
	s_mul_i32 s4, s4, 0x804
	s_add_i32 s4, s4, s38
	buffer_load_dword v16, v28, s[20:23], s4 offen nt
	buffer_load_dwordx3 v[40:42], v27, s[24:27], s9 offen nt
	buffer_load_dword v36, v28, s[16:19], s7 offen nt
	buffer_load_dword v37, v28, s[16:19], s8 offen nt
	s_waitcnt vmcnt(8)
	v_mov_b32_dpp v96, v12 wave_shr:1 row_mask:0xf bank_mask:0xf bound_ctrl:1
	v_mov_b32_dpp v97, v13 wave_shr:1 row_mask:0xf bank_mask:0xf bound_ctrl:1
	v_mov_b32_dpp v98, v14 wave_shr:1 row_mask:0xf bank_mask:0xf bound_ctrl:1
	v_mov_b32_dpp v100, v12 wave_shl:1 row_mask:0xf bank_mask:0xf bound_ctrl:1
	v_mov_b32_dpp v101, v13 wave_shl:1 row_mask:0xf bank_mask:0xf bound_ctrl:1
	v_mov_b32_dpp v102, v14 wave_shl:1 row_mask:0xf bank_mask:0xf bound_ctrl:1
	s_add_i32 s4, s34, 10
	s_cmpk_lt_u32 s4, 0x201
	s_cselect_b64 s[12:13], s[40:41], 0
	v_cmp_eq_u32_e64 s[14:15], s37, v2
	s_and_b64 s[14:15], s[14:15], s[12:13]
	v_cndmask_b32_e64 v29, 0, 1, s[14:15]
	v_mul_f32_e64 v62, v12, v12
	v_mul_f32_e64 v63, v12, v13
	v_mul_f32_e64 v92, v12, v14
	v_mul_f32_e64 v93, v13, v13
	v_mul_f32_e64 v110, v13, v14
	v_mul_f32_e64 v111, v14, v14
	v_or_b32_dpp v52, v29, v29 wave_shr:1 row_mask:0xf bank_mask:0xf bound_ctrl:1
	s_nop 1
	v_or_b32_dpp v52, v29, v52 wave_shl:1 row_mask:0xf bank_mask:0xf bound_ctrl:1
	s_nop 1
	v_or_b32_dpp v85, v52, v52 wave_shr:1 row_mask:0xf bank_mask:0xf bound_ctrl:1
	s_nop 1
	v_or_b32_dpp v85, v52, v85 wave_shl:1 row_mask:0xf bank_mask:0xf bound_ctrl:1
	v_or3_b32 v29, v85, v128, v129
	v_or3_b32 v29, v29, v53, v84
	s_add_i32 s4, s34, 7
	s_cmpk_lt_u32 s4, 0x1ff
	s_cselect_b64 s[12:13], s[42:43], 0
	v_cmp_ne_u32_e64 s[30:31], 0, v29
	s_and_b64 s[30:31], s[30:31], s[12:13]
	v_cndmask_b32_e64 v29, 0, 1.0, s[30:31]
	v_add_f32_e64 v120, v12, v96
	v_add_f32_e64 v121, v13, v97
	v_add_f32_e64 v122, v14, v98
	v_fma_f32 v62, v96, v96, v62
	v_fma_f32 v63, v96, v97, v63
	v_fma_f32 v92, v96, v98, v92
	v_fma_f32 v93, v97, v97, v93
	v_fma_f32 v110, v97, v98, v110
	v_fma_f32 v111, v98, v98, v111
	v_add_f32_dpp v133, v29, v29 wave_shr:1 row_mask:0xf bank_mask:0xf bound_ctrl:1
	v_add_f32_e64 v120, v120, v100
	v_add_f32_e64 v121, v121, v101
	v_add_f32_e64 v122, v122, v102
	v_fma_f32 v123, v100, v100, v62
	v_fma_f32 v126, v100, v101, v63
	v_fma_f32 v127, v100, v102, v92
	v_fma_f32 v130, v101, v101, v93
	v_fma_f32 v131, v101, v102, v110
	v_fma_f32 v132, v102, v102, v111
	v_add_f32_dpp v133, v29, v133 wave_shl:1 row_mask:0xf bank_mask:0xf bound_ctrl:1
	v_pk_add_f32 v[62:63], v[30:31], v[120:121]
	v_pk_add_f32 v[30:31], v[50:51], v[122:123]
	v_pk_add_f32 v[50:51], v[60:61], v[126:127]
	v_pk_add_f32 v[60:61], v[64:65], v[130:131]
	v_pk_add_f32 v[64:65], v[82:83], v[132:133]
	v_mul_f32_e64 v140, v62, v22
	v_mul_f32_e64 v141, v63, v22
	v_mul_f32_e64 v142, v30, v22
	v_fma_f32 v29, v31, v22, v26
	v_mul_f32_e64 v52, v50, v22
	v_mul_f32_e64 v82, v51, v22
	v_fma_f32 v83, v60, v22, v26
	v_mul_f32_e64 v92, v61, v22
	v_fma_f32 v93, v64, v22, v26
	v_fma_f32 v29, -v140, v140, v29
	v_fma_f32 v52, -v140, v141, v52
	v_fma_f32 v82, -v140, v142, v82
	v_fma_f32 v83, -v141, v141, v83
	v_fma_f32 v92, -v141, v142, v92
	v_fma_f32 v93, -v142, v142, v93
	v_mul_f32_e64 v110, v92, v92
	v_mul_f32_e64 v111, v52, v93
	v_mul_f32_e64 v156, v82, v83
	v_mul_f32_e64 v157, v82, v82
	v_mul_f32_e64 v158, v29, v92
	v_mul_f32_e64 v159, v52, v52
	v_fma_f32 v110, v83, v93, -v110
	v_fma_f32 v111, v82, v92, -v111
	v_fma_f32 v156, v52, v92, -v156
	v_fma_f32 v157, v29, v93, -v157
	v_fma_f32 v158, v52, v82, -v158
	v_fma_f32 v159, v29, v83, -v159
	v_mul_f32_e64 v160, v29, v110
	v_fma_f32 v160, v52, v111, v160
	v_fma_f32 v160, v82, v156, v160
	v_rcp_f32_e32 v160, v160
	v_cmp_ne_u32_e64 vcc, s37, v25
	v_mul_f32_e64 v160, v160, v22
	v_cndmask_b32_e64 v160, 0, v160, s[30:31]
	v_cndmask_b32_e64 v29, 0, v18, vcc
	v_cndmask_b32_e64 v149, 0, v22, s[30:31]
	v_mul_f32_e64 v143, v110, v160
	v_mul_f32_e64 v144, v111, v160
	v_mul_f32_e64 v145, v156, v160
	v_mul_f32_e64 v146, v157, v160
	v_mul_f32_e64 v147, v158, v160
	v_mul_f32_e64 v148, v159, v160
	v_add_f32_e64 v150, v65, v29
	v_mov_b32_e32 v151, v25
	ds_write_b128 v23, v[140:143] offset:3072
	ds_write_b128 v23, v[144:147] offset:4096
	ds_write_b128 v23, v[148:151] offset:5120
	v_mov_b32_dpp v30, v6 wave_shr:1 row_mask:0xf bank_mask:0xf bound_ctrl:1
	v_mov_b32_dpp v31, v7 wave_shr:1 row_mask:0xf bank_mask:0xf bound_ctrl:1
	v_mov_b32_dpp v50, v6 wave_shl:1 row_mask:0xf bank_mask:0xf bound_ctrl:1
	v_mov_b32_dpp v51, v7 wave_shl:1 row_mask:0xf bank_mask:0xf bound_ctrl:1
	v_pk_mul_f32 v[60:61], v[6:7], v[12:13] op_sel_hi:[1,0]
	v_pk_mul_f32 v[62:63], v[6:7], v[12:13] op_sel:[0,1]
	v_pk_mul_f32 v[64:65], v[6:7], v[14:15] op_sel_hi:[1,0]
	v_pk_add_f32 v[82:83], v[6:7], v[30:31]
	v_pk_fma_f32 v[60:61], v[30:31], v[96:97], v[60:61] op_sel_hi:[1,0,1]
	v_pk_fma_f32 v[62:63], v[30:31], v[96:97], v[62:63] op_sel:[0,1,0]
	v_pk_fma_f32 v[64:65], v[30:31], v[98:99], v[64:65] op_sel_hi:[1,0,1]
	v_pk_add_f32 v[82:83], v[82:83], v[50:51]
	v_pk_fma_f32 v[60:61], v[50:51], v[100:101], v[60:61] op_sel_hi:[1,0,1]
	v_pk_fma_f32 v[62:63], v[50:51], v[100:101], v[62:63] op_sel:[0,1,0]
	v_pk_fma_f32 v[64:65], v[50:51], v[102:103], v[64:65] op_sel_hi:[1,0,1]
	s_waitcnt lgkmcnt(0)
	s_barrier
	v_pk_add_f32 v[30:31], v[38:39], v[82:83]
	v_pk_add_f32 v[38:39], v[94:95], v[60:61]
	v_pk_add_f32 v[50:51], v[56:57], v[62:63]
	v_pk_add_f32 v[56:57], v[66:67], v[64:65]
	v_pk_fma_f32 v[38:39], v[140:141], v[30:31], v[38:39] op_sel_hi:[0,1,1] neg_lo:[1,0,0] neg_hi:[1,0,0]
	v_pk_fma_f32 v[50:51], v[140:141], v[30:31], v[50:51] op_sel:[1,0,0] neg_lo:[1,0,0] neg_hi:[1,0,0]
	v_pk_fma_f32 v[56:57], v[142:143], v[30:31], v[56:57] op_sel_hi:[0,1,1] neg_lo:[1,0,0] neg_hi:[1,0,0]
	v_pk_mul_f32 v[66:67], v[142:143], v[38:39] op_sel:[1,0]
	v_pk_mul_f32 v[92:93], v[144:145], v[38:39] op_sel_hi:[0,1]
	v_pk_mul_f32 v[94:95], v[144:145], v[38:39] op_sel:[1,0]
	v_pk_fma_f32 v[66:67], v[144:145], v[50:51], v[66:67] op_sel_hi:[0,1,1]
	v_pk_fma_f32 v[92:93], v[146:147], v[50:51], v[92:93] op_sel_hi:[0,1,1]
	v_pk_fma_f32 v[94:95], v[146:147], v[50:51], v[94:95] op_sel:[1,0,0]
	v_pk_fma_f32 v[66:67], v[144:145], v[56:57], v[66:67] op_sel:[1,0,0]
	v_pk_fma_f32 v[92:93], v[146:147], v[56:57], v[92:93] op_sel:[1,0,0]
	v_pk_fma_f32 v[94:95], v[148:149], v[56:57], v[94:95] op_sel_hi:[0,1,1]
	v_pk_mul_f32 v[110:111], v[140:141], v[66:67] op_sel_hi:[0,1]
	v_pk_fma_f32 v[110:111], v[140:141], v[92:93], v[110:111] op_sel:[1,0,0]
	v_pk_fma_f32 v[110:111], v[142:143], v[94:95], v[110:111] op_sel_hi:[0,1,1]
	v_pk_fma_f32 v[110:111], v[148:149], v[30:31], v[110:111] op_sel:[1,0,0] neg_lo:[0,0,1] neg_hi:[0,0,1]
	v_cmp_eq_u32_e64 s[10:11], 6, v151
	v_cmp_eq_u32_e64 s[14:15], 7, v151
	v_pk_add_f32 v[30:31], v[58:59], v[66:67]
	v_pk_add_f32 v[38:39], v[88:89], v[92:93]
	v_pk_add_f32 v[50:51], v[108:109], v[94:95]
	v_pk_add_f32 v[56:57], v[118:119], v[110:111]
	v_pk_fma_f32 v[58:59], v[44:45], v[30:31], v[56:57] op_sel_hi:[0,1,1]
	v_pk_fma_f32 v[88:89], v[68:69], v[30:31], v[56:57] op_sel_hi:[0,1,1]
	v_pk_fma_f32 v[58:59], v[44:45], v[38:39], v[58:59] op_sel:[1,0,0]
	v_pk_fma_f32 v[88:89], v[68:69], v[38:39], v[88:89] op_sel:[1,0,0]
	v_pk_fma_f32 v[58:59], v[46:47], v[50:51], v[58:59] op_sel_hi:[0,1,1]
	v_pk_fma_f32 v[88:89], v[70:71], v[50:51], v[88:89] op_sel_hi:[0,1,1]
	v_pk_fma_f32 v[56:57], v[72:73], v[30:31], v[56:57] op_sel_hi:[0,1,1]
	v_pk_fma_f32 v[56:57], v[72:73], v[38:39], v[56:57] op_sel:[1,0,0]
	v_pk_fma_f32 v[56:57], v[74:75], v[50:51], v[56:57] op_sel_hi:[0,1,1]
	v_cndmask_b32_e64 v108, 0, v18, s[10:11]
	v_cndmask_b32_e64 v109, 0, v18, s[14:15]
	v_add_f32_dpp v56, v58, v56 wave_shl:1 row_mask:0xf bank_mask:0xf bound_ctrl:1
	v_add_f32_dpp v57, v59, v57 wave_shl:1 row_mask:0xf bank_mask:0xf bound_ctrl:1
	s_add_i32 s4, s34, 7
	s_cmpk_lt_i32 s4, 0x201
	s_cselect_b64 s[12:13], s[0:1], 0
	v_add_f32_dpp v56, v88, v56 wave_shr:1 row_mask:0xf bank_mask:0xf bound_ctrl:1
	v_add_f32_dpp v57, v89, v57 wave_shr:1 row_mask:0xf bank_mask:0xf bound_ctrl:1
	v_pk_fma_f32 v[56:57], v[48:49], v[150:151], v[56:57] op_sel_hi:[1,0,1] neg_lo:[0,0,1] neg_hi:[0,0,1]
	v_pk_add_f32 v[56:57], v[56:57], v[108:109] neg_lo:[0,1] neg_hi:[0,1]
	v_pk_mul_f32 v[118:119], v[56:57], v[56:57]
	v_add_f32_e32 v118, v118, v119
	v_cndmask_b32_e64 v119, 0, v118, s[12:13]
	v_add_f32_e32 v1, v1, v119
	s_waitcnt vmcnt(4)
	v_mov_b32_dpp v44, v32 wave_shr:1 row_mask:0xf bank_mask:0xf bound_ctrl:1
	v_mov_b32_dpp v45, v33 wave_shr:1 row_mask:0xf bank_mask:0xf bound_ctrl:1
	v_mov_b32_dpp v46, v34 wave_shr:1 row_mask:0xf bank_mask:0xf bound_ctrl:1
	v_mov_b32_dpp v48, v32 wave_shl:1 row_mask:0xf bank_mask:0xf bound_ctrl:1
	v_mov_b32_dpp v49, v33 wave_shl:1 row_mask:0xf bank_mask:0xf bound_ctrl:1
	v_mov_b32_dpp v50, v34 wave_shl:1 row_mask:0xf bank_mask:0xf bound_ctrl:1
	s_add_i32 s4, s34, 11
	s_cmpk_lt_u32 s4, 0x201
	s_cselect_b64 s[12:13], s[40:41], 0
	v_cmp_eq_u32_e64 s[14:15], s37, v3
	s_and_b64 s[14:15], s[14:15], s[12:13]
	v_cndmask_b32_e64 v25, 0, 1, s[14:15]
	v_mul_f32_e64 v30, v32, v32
	v_mul_f32_e64 v31, v32, v33
	v_mul_f32_e64 v38, v32, v34
	v_mul_f32_e64 v39, v33, v33
	v_mul_f32_e64 v56, v33, v34
	v_mul_f32_e64 v57, v34, v34
	v_or_b32_dpp v29, v25, v25 wave_shr:1 row_mask:0xf bank_mask:0xf bound_ctrl:1
	s_nop 1
	v_or_b32_dpp v29, v25, v29 wave_shl:1 row_mask:0xf bank_mask:0xf bound_ctrl:1
	s_nop 1
	v_or_b32_dpp v52, v29, v29 wave_shr:1 row_mask:0xf bank_mask:0xf bound_ctrl:1
	s_nop 1
	v_or_b32_dpp v52, v29, v52 wave_shl:1 row_mask:0xf bank_mask:0xf bound_ctrl:1
	v_or3_b32 v25, v52, v85, v128
	v_or3_b32 v25, v25, v129, v53
	s_add_i32 s4, s34, 8
	s_cmpk_lt_u32 s4, 0x1ff
	s_cselect_b64 s[12:13], s[42:43], 0
	v_cmp_ne_u32_e64 s[30:31], 0, v25
	s_and_b64 s[30:31], s[30:31], s[12:13]
	v_cndmask_b32_e64 v25, 0, 1.0, s[30:31]
	v_add_f32_e64 v58, v32, v44
	v_add_f32_e64 v59, v33, v45
	v_add_f32_e64 v68, v34, v46
	v_fma_f32 v30, v44, v44, v30
	v_fma_f32 v31, v44, v45, v31
	v_fma_f32 v38, v44, v46, v38
	v_fma_f32 v39, v45, v45, v39
	v_fma_f32 v56, v45, v46, v56
	v_fma_f32 v57, v46, v46, v57
	v_add_f32_dpp v75, v25, v25 wave_shr:1 row_mask:0xf bank_mask:0xf bound_ctrl:1
	v_add_f32_e64 v58, v58, v48
	v_add_f32_e64 v59, v59, v49
	v_add_f32_e64 v68, v68, v50
	v_fma_f32 v69, v48, v48, v30
	v_fma_f32 v70, v48, v49, v31
	v_fma_f32 v71, v48, v50, v38
	v_fma_f32 v72, v49, v49, v39
	v_fma_f32 v73, v49, v50, v56
	v_fma_f32 v74, v50, v50, v57
	v_add_f32_dpp v75, v25, v75 wave_shl:1 row_mask:0xf bank_mask:0xf bound_ctrl:1
	v_pk_add_f32 v[30:31], v[120:121], v[58:59]
	v_pk_add_f32 v[38:39], v[54:55], v[30:31]
	v_pk_add_f32 v[54:55], v[122:123], v[68:69]
	v_pk_add_f32 v[56:57], v[80:81], v[54:55]
	v_pk_add_f32 v[80:81], v[126:127], v[70:71]
	v_pk_add_f32 v[88:89], v[90:91], v[80:81]
	v_pk_add_f32 v[90:91], v[130:131], v[72:73]
	v_pk_add_f32 v[108:109], v[116:117], v[90:91]
	v_pk_add_f32 v[116:117], v[132:133], v[74:75]
	v_pk_add_f32 v[118:119], v[124:125], v[116:117]
	v_mul_f32_e64 v120, v38, v22
	v_mul_f32_e64 v121, v39, v22
	v_mul_f32_e64 v122, v56, v22
	v_fma_f32 v25, v57, v22, v26
	v_mul_f32_e64 v29, v88, v22
	v_mul_f32_e64 v84, v89, v22
	v_fma_f32 v130, v108, v22, v26
	v_mul_f32_e64 v131, v109, v22
	v_fma_f32 v132, v118, v22, v26
	v_fma_f32 v25, -v120, v120, v25
	v_fma_f32 v29, -v120, v121, v29
	v_fma_f32 v84, -v120, v122, v84
	v_fma_f32 v130, -v121, v121, v130
	v_fma_f32 v131, -v121, v122, v131
	v_fma_f32 v132, -v122, v122, v132
	v_mul_f32_e64 v133, v131, v131
	v_mul_f32_e64 v144, v29, v132
	v_mul_f32_e64 v145, v84, v130
	v_mul_f32_e64 v146, v84, v84
	v_mul_f32_e64 v147, v25, v131
	v_mul_f32_e64 v148, v29, v29
	v_fma_f32 v133, v130, v132, -v133
	v_fma_f32 v144, v84, v131, -v144
	v_fma_f32 v145, v29, v131, -v145
	v_fma_f32 v146, v25, v132, -v146
	v_fma_f32 v147, v29, v84, -v147
	v_fma_f32 v148, v25, v130, -v148
	v_mul_f32_e64 v149, v25, v133
	v_fma_f32 v149, v29, v144, v149
	v_fma_f32 v149, v84, v145, v149
	v_rcp_f32_e32 v149, v149
	v_cmp_ne_u32_e64 vcc, s37, v24
	v_mul_f32_e64 v149, v149, v22
	v_cndmask_b32_e64 v149, 0, v149, s[30:31]
	v_cndmask_b32_e64 v25, 0, v18, vcc
	v_cndmask_b32_e64 v141, 0, v22, s[30:31]
	v_mul_f32_e64 v123, v133, v149
	v_mul_f32_e64 v124, v144, v149
	v_mul_f32_e64 v125, v145, v149
	v_mul_f32_e64 v126, v146, v149
	v_mul_f32_e64 v127, v147, v149
	v_mul_f32_e64 v140, v148, v149
	v_add_f32_e64 v142, v119, v25
	v_mov_b32_e32 v143, v24
	ds_write_b128 v23, v[120:123]
	ds_write_b128 v23, v[124:127] offset:1024
	ds_write_b128 v23, v[140:143] offset:2048
	v_mov_b32_dpp v24, v20 wave_shr:1 row_mask:0xf bank_mask:0xf bound_ctrl:1
	v_mov_b32_dpp v25, v21 wave_shr:1 row_mask:0xf bank_mask:0xf bound_ctrl:1
	v_mov_b32_dpp v38, v20 wave_shl:1 row_mask:0xf bank_mask:0xf bound_ctrl:1
	v_mov_b32_dpp v39, v21 wave_shl:1 row_mask:0xf bank_mask:0xf bound_ctrl:1
	v_pk_mul_f32 v[56:57], v[20:21], v[32:33] op_sel_hi:[1,0]
	v_pk_mul_f32 v[88:89], v[20:21], v[32:33] op_sel:[0,1]
	v_pk_mul_f32 v[108:109], v[20:21], v[34:35] op_sel_hi:[1,0]
	v_pk_add_f32 v[118:119], v[20:21], v[24:25]
	v_pk_fma_f32 v[56:57], v[24:25], v[44:45], v[56:57] op_sel_hi:[1,0,1]
	v_pk_fma_f32 v[88:89], v[24:25], v[44:45], v[88:89] op_sel:[0,1,0]
	v_pk_fma_f32 v[108:109], v[24:25], v[46:47], v[108:109] op_sel_hi:[1,0,1]
	v_pk_add_f32 v[118:119], v[118:119], v[38:39]
	v_pk_fma_f32 v[56:57], v[38:39], v[48:49], v[56:57] op_sel_hi:[1,0,1]
	v_pk_fma_f32 v[88:89], v[38:39], v[48:49], v[88:89] op_sel:[0,1,0]
	v_pk_fma_f32 v[108:109], v[38:39], v[50:51], v[108:109] op_sel_hi:[1,0,1]
	s_waitcnt lgkmcnt(0)
	s_barrier
	v_pk_add_f32 v[24:25], v[82:83], v[118:119]
	v_pk_add_f32 v[38:39], v[138:139], v[24:25]
	v_pk_add_f32 v[82:83], v[60:61], v[56:57]
	v_pk_add_f32 v[130:131], v[112:113], v[82:83]
	v_pk_add_f32 v[60:61], v[62:63], v[88:89]
	v_pk_add_f32 v[112:113], v[134:135], v[60:61]
	v_pk_add_f32 v[62:63], v[64:65], v[108:109]
	v_pk_add_f32 v[132:133], v[136:137], v[62:63]
	v_pk_fma_f32 v[130:131], v[120:121], v[38:39], v[130:131] op_sel_hi:[0,1,1] neg_lo:[1,0,0] neg_hi:[1,0,0]
	v_pk_fma_f32 v[112:113], v[120:121], v[38:39], v[112:113] op_sel:[1,0,0] neg_lo:[1,0,0] neg_hi:[1,0,0]
	v_pk_fma_f32 v[132:133], v[122:123], v[38:39], v[132:133] op_sel_hi:[0,1,1] neg_lo:[1,0,0] neg_hi:[1,0,0]
	v_pk_mul_f32 v[64:65], v[122:123], v[130:131] op_sel:[1,0]
	v_pk_mul_f32 v[134:135], v[124:125], v[130:131] op_sel_hi:[0,1]
	v_pk_mul_f32 v[136:137], v[124:125], v[130:131] op_sel:[1,0]
	v_pk_fma_f32 v[64:65], v[124:125], v[112:113], v[64:65] op_sel_hi:[0,1,1]
	v_pk_fma_f32 v[134:135], v[126:127], v[112:113], v[134:135] op_sel_hi:[0,1,1]
	v_pk_fma_f32 v[136:137], v[126:127], v[112:113], v[136:137] op_sel:[1,0,0]
	v_pk_fma_f32 v[64:65], v[124:125], v[132:133], v[64:65] op_sel:[1,0,0]
	v_pk_fma_f32 v[134:135], v[126:127], v[132:133], v[134:135] op_sel:[1,0,0]
	v_pk_fma_f32 v[136:137], v[140:141], v[132:133], v[136:137] op_sel_hi:[0,1,1]
	v_pk_mul_f32 v[138:139], v[120:121], v[64:65] op_sel_hi:[0,1]
	v_pk_fma_f32 v[138:139], v[120:121], v[134:135], v[138:139] op_sel:[1,0,0]
	v_pk_fma_f32 v[138:139], v[122:123], v[136:137], v[138:139] op_sel_hi:[0,1,1]
	v_pk_fma_f32 v[138:139], v[140:141], v[38:39], v[138:139] op_sel:[1,0,0] neg_lo:[0,0,1] neg_hi:[0,0,1]
	v_cmp_eq_u32_e64 s[10:11], 6, v143
	v_cmp_eq_u32_e64 s[14:15], 7, v143
	v_pk_add_f32 v[38:39], v[66:67], v[64:65]
	v_pk_add_f32 v[112:113], v[86:87], v[38:39]
	v_pk_add_f32 v[66:67], v[92:93], v[134:135]
	v_pk_add_f32 v[86:87], v[114:115], v[66:67]
	v_pk_add_f32 v[92:93], v[94:95], v[136:137]
	v_pk_add_f32 v[114:115], v[152:153], v[92:93]
	v_pk_add_f32 v[94:95], v[110:111], v[138:139]
	v_pk_add_f32 v[130:131], v[154:155], v[94:95]
	v_pk_fma_f32 v[110:111], v[76:77], v[112:113], v[130:131] op_sel_hi:[0,1,1]
	v_pk_fma_f32 v[132:133], v[104:105], v[112:113], v[130:131] op_sel_hi:[0,1,1]
	v_pk_fma_f32 v[110:111], v[76:77], v[86:87], v[110:111] op_sel:[1,0,0]
	v_pk_fma_f32 v[132:133], v[104:105], v[86:87], v[132:133] op_sel:[1,0,0]
	v_pk_fma_f32 v[110:111], v[78:79], v[114:115], v[110:111] op_sel_hi:[0,1,1]
	v_pk_fma_f32 v[132:133], v[106:107], v[114:115], v[132:133] op_sel_hi:[0,1,1]
	v_pk_fma_f32 v[130:131], v[8:9], v[112:113], v[130:131] op_sel_hi:[0,1,1]
	v_pk_fma_f32 v[130:131], v[8:9], v[86:87], v[130:131] op_sel:[1,0,0]
	v_pk_fma_f32 v[130:131], v[10:11], v[114:115], v[130:131] op_sel_hi:[0,1,1]
	v_cndmask_b32_e64 v144, 0, v18, s[10:11]
	v_cndmask_b32_e64 v145, 0, v18, s[14:15]
	v_add_f32_dpp v130, v110, v130 wave_shl:1 row_mask:0xf bank_mask:0xf bound_ctrl:1
	v_add_f32_dpp v131, v111, v131 wave_shl:1 row_mask:0xf bank_mask:0xf bound_ctrl:1
	s_add_i32 s4, s34, 8
	s_cmpk_lt_i32 s4, 0x201
	s_cselect_b64 s[12:13], s[0:1], 0
	v_add_f32_dpp v130, v132, v130 wave_shr:1 row_mask:0xf bank_mask:0xf bound_ctrl:1
	v_add_f32_dpp v131, v133, v131 wave_shr:1 row_mask:0xf bank_mask:0xf bound_ctrl:1
	v_pk_fma_f32 v[130:131], v[4:5], v[142:143], v[130:131] op_sel_hi:[1,0,1] neg_lo:[0,0,1] neg_hi:[0,0,1]
	v_pk_add_f32 v[130:131], v[130:131], v[144:145] neg_lo:[0,1] neg_hi:[0,1]
	v_pk_mul_f32 v[146:147], v[130:131], v[130:131]
	v_add_f32_e32 v146, v146, v147
	v_cndmask_b32_e64 v147, 0, v146, s[12:13]
	v_add_f32_e32 v1, v1, v147
	s_waitcnt vmcnt(0)
	v_mov_b32_dpp v8, v40 wave_shr:1 row_mask:0xf bank_mask:0xf bound_ctrl:1
	v_mov_b32_dpp v9, v41 wave_shr:1 row_mask:0xf bank_mask:0xf bound_ctrl:1
	v_mov_b32_dpp v10, v42 wave_shr:1 row_mask:0xf bank_mask:0xf bound_ctrl:1
	v_mov_b32_dpp v76, v40 wave_shl:1 row_mask:0xf bank_mask:0xf bound_ctrl:1
	v_mov_b32_dpp v77, v41 wave_shl:1 row_mask:0xf bank_mask:0xf bound_ctrl:1
	v_mov_b32_dpp v78, v42 wave_shl:1 row_mask:0xf bank_mask:0xf bound_ctrl:1
	s_add_i32 s4, s34, 12
	s_cmpk_lt_u32 s4, 0x201
	s_cselect_b64 s[12:13], s[40:41], 0
	v_cmp_eq_u32_e64 s[14:15], s37, v16
	s_and_b64 s[14:15], s[14:15], s[12:13]
	v_cndmask_b32_e64 v29, 0, 1, s[14:15]
	v_mul_f32_e64 v4, v40, v40
	v_mul_f32_e64 v5, v40, v41
	v_mul_f32_e64 v86, v40, v42
	v_mul_f32_e64 v87, v41, v41
	v_mul_f32_e64 v104, v41, v42
	v_mul_f32_e64 v105, v42, v42
	v_or_b32_dpp v53, v29, v29 wave_shr:1 row_mask:0xf bank_mask:0xf bound_ctrl:1
	s_nop 1
	v_or_b32_dpp v53, v29, v53 wave_shl:1 row_mask:0xf bank_mask:0xf bound_ctrl:1
	s_nop 1
	v_or_b32_dpp v84, v53, v53 wave_shr:1 row_mask:0xf bank_mask:0xf bound_ctrl:1
	s_nop 1
	v_or_b32_dpp v84, v53, v84 wave_shl:1 row_mask:0xf bank_mask:0xf bound_ctrl:1
	v_or3_b32 v29, v84, v52, v85
	v_or3_b32 v29, v29, v128, v129
	s_add_i32 s4, s34, 9
	s_cmpk_lt_u32 s4, 0x1ff
	s_cselect_b64 s[12:13], s[42:43], 0
	v_cmp_ne_u32_e64 s[30:31], 0, v29
	s_and_b64 s[30:31], s[30:31], s[12:13]
	v_cndmask_b32_e64 v29, 0, 1.0, s[30:31]
	v_add_f32_e64 v106, v40, v8
	v_add_f32_e64 v107, v41, v9
	v_add_f32_e64 v110, v42, v10
	v_fma_f32 v4, v8, v8, v4
	v_fma_f32 v5, v8, v9, v5
	v_fma_f32 v86, v8, v10, v86
	v_fma_f32 v87, v9, v9, v87
	v_fma_f32 v104, v9, v10, v104
	v_fma_f32 v105, v10, v10, v105
	v_add_f32_dpp v121, v29, v29 wave_shr:1 row_mask:0xf bank_mask:0xf bound_ctrl:1
	v_add_f32_e64 v106, v106, v76
	v_add_f32_e64 v107, v107, v77
	v_add_f32_e64 v110, v110, v78
	v_fma_f32 v111, v76, v76, v4
	v_fma_f32 v112, v76, v77, v5
	v_fma_f32 v113, v76, v78, v86
	v_fma_f32 v114, v77, v77, v87
	v_fma_f32 v115, v77, v78, v104
	v_fma_f32 v120, v78, v78, v105
	v_add_f32_dpp v121, v29, v121 wave_shl:1 row_mask:0xf bank_mask:0xf bound_ctrl:1
	v_pk_add_f32 v[4:5], v[30:31], v[106:107]
	v_pk_add_f32 v[30:31], v[54:55], v[110:111]
	v_pk_add_f32 v[54:55], v[80:81], v[112:113]
	v_pk_add_f32 v[80:81], v[90:91], v[114:115]
	v_pk_add_f32 v[86:87], v[116:117], v[120:121]
	v_mul_f32_e64 v124, v4, v22
	v_mul_f32_e64 v125, v5, v22
	v_mul_f32_e64 v126, v30, v22
	v_fma_f32 v29, v31, v22, v26
	v_mul_f32_e64 v53, v54, v22
	v_mul_f32_e64 v90, v55, v22
	v_fma_f32 v91, v80, v22, v26
	v_mul_f32_e64 v104, v81, v22
	v_fma_f32 v105, v86, v22, v26
	v_fma_f32 v29, -v124, v124, v29
	v_fma_f32 v53, -v124, v125, v53
	v_fma_f32 v90, -v124, v126, v90
	v_fma_f32 v91, -v125, v125, v91
	v_fma_f32 v104, -v125, v126, v104
	v_fma_f32 v105, -v126, v126, v105
	v_mul_f32_e64 v116, v104, v104
	v_mul_f32_e64 v117, v53, v105
	v_mul_f32_e64 v122, v90, v91
	v_mul_f32_e64 v123, v90, v90
	v_mul_f32_e64 v130, v29, v104
	v_mul_f32_e64 v131, v53, v53
	v_fma_f32 v116, v91, v105, -v116
	v_fma_f32 v117, v90, v104, -v117
	v_fma_f32 v122, v53, v104, -v122
	v_fma_f32 v123, v29, v105, -v123
	v_fma_f32 v130, v53, v90, -v130
	v_fma_f32 v131, v29, v91, -v131
	v_mul_f32_e64 v132, v29, v116
	v_fma_f32 v132, v53, v117, v132
	v_fma_f32 v132, v90, v122, v132
	v_rcp_f32_e32 v132, v132
	v_cmp_ne_u32_e64 vcc, s37, v17
	v_mul_f32_e64 v132, v132, v22
	v_cndmask_b32_e64 v132, 0, v132, s[30:31]
	v_cndmask_b32_e64 v29, 0, v18, vcc
	v_cndmask_b32_e64 v145, 0, v22, s[30:31]
	v_mul_f32_e64 v127, v116, v132
	v_mul_f32_e64 v140, v117, v132
	v_mul_f32_e64 v141, v122, v132
	v_mul_f32_e64 v142, v123, v132
	v_mul_f32_e64 v143, v130, v132
	v_mul_f32_e64 v144, v131, v132
	v_add_f32_e64 v146, v87, v29
	v_mov_b32_e32 v147, v17
	ds_write_b128 v23, v[124:127] offset:3072
	ds_write_b128 v23, v[140:143] offset:4096
	ds_write_b128 v23, v[144:147] offset:5120
	v_mov_b32_dpp v4, v36 wave_shr:1 row_mask:0xf bank_mask:0xf bound_ctrl:1
	v_mov_b32_dpp v5, v37 wave_shr:1 row_mask:0xf bank_mask:0xf bound_ctrl:1
	v_mov_b32_dpp v30, v36 wave_shl:1 row_mask:0xf bank_mask:0xf bound_ctrl:1
	v_mov_b32_dpp v31, v37 wave_shl:1 row_mask:0xf bank_mask:0xf bound_ctrl:1
	v_pk_mul_f32 v[54:55], v[36:37], v[40:41] op_sel_hi:[1,0]
	v_pk_mul_f32 v[80:81], v[36:37], v[40:41] op_sel:[0,1]
	v_pk_mul_f32 v[86:87], v[36:37], v[42:43] op_sel_hi:[1,0]
	v_pk_add_f32 v[90:91], v[36:37], v[4:5]
	v_pk_fma_f32 v[54:55], v[4:5], v[8:9], v[54:55] op_sel_hi:[1,0,1]
	v_pk_fma_f32 v[80:81], v[4:5], v[8:9], v[80:81] op_sel:[0,1,0]
	v_pk_fma_f32 v[86:87], v[4:5], v[10:11], v[86:87] op_sel_hi:[1,0,1]
	v_pk_add_f32 v[90:91], v[90:91], v[30:31]
	v_pk_fma_f32 v[54:55], v[30:31], v[76:77], v[54:55] op_sel_hi:[1,0,1]
	v_pk_fma_f32 v[80:81], v[30:31], v[76:77], v[80:81] op_sel:[0,1,0]
	v_pk_fma_f32 v[86:87], v[30:31], v[78:79], v[86:87] op_sel_hi:[1,0,1]
	s_waitcnt lgkmcnt(0)
	s_barrier
	v_pk_add_f32 v[4:5], v[24:25], v[90:91]
	v_pk_add_f32 v[24:25], v[82:83], v[54:55]
	v_pk_add_f32 v[30:31], v[60:61], v[80:81]
	v_pk_add_f32 v[60:61], v[62:63], v[86:87]
	v_pk_fma_f32 v[24:25], v[124:125], v[4:5], v[24:25] op_sel_hi:[0,1,1] neg_lo:[1,0,0] neg_hi:[1,0,0]
	v_pk_fma_f32 v[30:31], v[124:125], v[4:5], v[30:31] op_sel:[1,0,0] neg_lo:[1,0,0] neg_hi:[1,0,0]
	v_pk_fma_f32 v[60:61], v[126:127], v[4:5], v[60:61] op_sel_hi:[0,1,1] neg_lo:[1,0,0] neg_hi:[1,0,0]
	v_pk_mul_f32 v[62:63], v[126:127], v[24:25] op_sel:[1,0]
	v_pk_mul_f32 v[82:83], v[140:141], v[24:25] op_sel_hi:[0,1]
	v_pk_mul_f32 v[104:105], v[140:141], v[24:25] op_sel:[1,0]
	v_pk_fma_f32 v[62:63], v[140:141], v[30:31], v[62:63] op_sel_hi:[0,1,1]
	v_pk_fma_f32 v[82:83], v[142:143], v[30:31], v[82:83] op_sel_hi:[0,1,1]
	v_pk_fma_f32 v[104:105], v[142:143], v[30:31], v[104:105] op_sel:[1,0,0]
	v_pk_fma_f32 v[62:63], v[140:141], v[60:61], v[62:63] op_sel:[1,0,0]
	v_pk_fma_f32 v[82:83], v[142:143], v[60:61], v[82:83] op_sel:[1,0,0]
	v_pk_fma_f32 v[104:105], v[144:145], v[60:61], v[104:105] op_sel_hi:[0,1,1]
	v_pk_mul_f32 v[116:117], v[124:125], v[62:63] op_sel_hi:[0,1]
	v_pk_fma_f32 v[116:117], v[124:125], v[82:83], v[116:117] op_sel:[1,0,0]
	v_pk_fma_f32 v[116:117], v[126:127], v[104:105], v[116:117] op_sel_hi:[0,1,1]
	v_pk_fma_f32 v[116:117], v[144:145], v[4:5], v[116:117] op_sel:[1,0,0] neg_lo:[0,0,1] neg_hi:[0,0,1]
	v_cmp_eq_u32_e64 s[10:11], 6, v147
	v_cmp_eq_u32_e64 s[14:15], 7, v147
	v_pk_add_f32 v[4:5], v[38:39], v[62:63]
	v_pk_add_f32 v[24:25], v[66:67], v[82:83]
	v_pk_add_f32 v[30:31], v[92:93], v[104:105]
	v_pk_add_f32 v[38:39], v[94:95], v[116:117]
	v_pk_fma_f32 v[60:61], v[96:97], v[4:5], v[38:39] op_sel_hi:[0,1,1]
	v_pk_fma_f32 v[66:67], v[100:101], v[4:5], v[38:39] op_sel_hi:[0,1,1]
	v_pk_fma_f32 v[60:61], v[96:97], v[24:25], v[60:61] op_sel:[1,0,0]
	v_pk_fma_f32 v[66:67], v[100:101], v[24:25], v[66:67] op_sel:[1,0,0]
	v_pk_fma_f32 v[60:61], v[98:99], v[30:31], v[60:61] op_sel_hi:[0,1,1]
	v_pk_fma_f32 v[66:67], v[102:103], v[30:31], v[66:67] op_sel_hi:[0,1,1]
	v_pk_fma_f32 v[38:39], v[12:13], v[4:5], v[38:39] op_sel_hi:[0,1,1]
	v_pk_fma_f32 v[38:39], v[12:13], v[24:25], v[38:39] op_sel:[1,0,0]
	v_pk_fma_f32 v[38:39], v[14:15], v[30:31], v[38:39] op_sel_hi:[0,1,1]
	v_cndmask_b32_e64 v92, 0, v18, s[10:11]
	v_cndmask_b32_e64 v93, 0, v18, s[14:15]
	v_add_f32_dpp v38, v60, v38 wave_shl:1 row_mask:0xf bank_mask:0xf bound_ctrl:1
	v_add_f32_dpp v39, v61, v39 wave_shl:1 row_mask:0xf bank_mask:0xf bound_ctrl:1
	s_add_i32 s4, s34, 9
	s_cmpk_lt_i32 s4, 0x201
	s_cselect_b64 s[12:13], s[0:1], 0
	v_add_f32_dpp v38, v66, v38 wave_shr:1 row_mask:0xf bank_mask:0xf bound_ctrl:1
	v_add_f32_dpp v39, v67, v39 wave_shr:1 row_mask:0xf bank_mask:0xf bound_ctrl:1
	v_pk_fma_f32 v[38:39], v[6:7], v[146:147], v[38:39] op_sel_hi:[1,0,1] neg_lo:[0,0,1] neg_hi:[0,0,1]
	v_pk_add_f32 v[38:39], v[38:39], v[92:93] neg_lo:[0,1] neg_hi:[0,1]
	v_pk_mul_f32 v[94:95], v[38:39], v[38:39]
	v_add_f32_e32 v94, v94, v95
	v_cndmask_b32_e64 v95, 0, v94, s[12:13]
	v_add_f32_e32 v1, v1, v95
	v_mov_b32_e32 v0, v1
	s_branch .LBB0_29
